# norm phases (layer-0 combine+norm, final norm): loop-invariant gain chunks loaded once before the row loop; the 8-step gain-load/vmcnt(0)/store ladders per row become wait-free multiplies + stores (on
# speedup vs baseline: 1.0080x; 1.0080x over previous
; #define GAS __attribute__((address_space(1)))
; __device__ __forceinline__ float bflo(unsigned w) { return __uint_as_float(w << 16); }
; __device__ __forceinline__ float bfhi(unsigned w) { return __uint_as_float(w & 0xffff0000u); }
; template <int MODE, bool W8 = false>
; __device__ __forceinline__ void norm_rows(const Ctx& C, const void* src, bf16* xdst, const unsigned char* YS8, const int* srow, const float* gate, const float* gain, bf16* XN, float* outf, unsigned char* XN8 = nullptr) {
;     ...
;     for (int m0 = C.gw; m0 < T; m0 += NR * C.NGW) {
;         f32x4 v[NR][8]; unsigned ya[NR][8], yb[NR][8]; float h0[NR], h1[NR];
; #pragma unroll
;         for (int q = 0; q < NR; ++q) { const int m = m0 + q * C.NGW;
;             if (MODE == 0) { const GAS f32x4* xr = (const GAS f32x4*)((const float*)src + (size_t)m * DM) + C.lane;
; #pragma unroll
;                 for (int j = 0; j < 8; ++j) v[q][j] = xr[64 * j]; }
;             else { const GAS v2u* xr = (const GAS v2u*)((const bf16*)src + (size_t)m * DM) + C.lane;
; #pragma unroll
;                 for (int j = 0; j < 8; ++j) { const v2u t_ = xr[64 * j]; v[q][j] = (f32x4){bflo(t_.x), bfhi(t_.x), bflo(t_.y), bfhi(t_.y)}; } }
;             if (MODE >= 1) {
;                 h0[q] = gate[2 * m] * (1.0f / SY); h1[q] = gate[2 * m + 1] * (1.0f / SY);
;                 const GAS unsigned* y0 = (const GAS unsigned*)(YS8 + (size_t)srow[2 * m] * DM) + C.lane; const GAS unsigned* y1 = (const GAS unsigned*)(YS8 + (size_t)srow[2 * m + 1] * DM) + C.lane;
; #pragma unroll
;                 for (int j = 0; j < 8; ++j) { ya[q][j] = y0[64 * j]; yb[q][j] = y1[64 * j]; } } }
;     ...
;             const GAS f32x4* gg = (const GAS f32x4*)gain + C.lane;
.LBB0_1318:
	v_readlane_b32 s0, v253, 16
	s_waitcnt vmcnt(0)
	v_mbcnt_lo_u32_b32 v16, -1, 0
	v_mbcnt_hi_u32_b32 v16, -1, v16
	v_readlane_b32 s1, v253, 18
	v_readlane_b32 s16, v253, 8
	v_add_u32_e32 v0, s0, v16
	v_readlane_b32 s0, v253, 19
	s_mov_b32 s6, s1
	v_readlane_b32 s1, v253, 17
	v_add_u32_e32 v1, s0, v0
	v_readlane_b32 s0, v253, 0
	v_readlane_b32 s18, v253, 10
	v_readlane_b32 s19, v253, 11
	s_mov_b64 s[4:5], s[18:19]
	s_add_u32 s0, s4, 0x62800000
	v_readlane_b32 s22, v253, 14
	s_addc_u32 s1, s5, 0
	v_readlane_b32 s23, v253, 15
	s_add_u32 s22, s4, 0x6a820000
	s_addc_u32 s23, s5, 0
	s_add_u32 s24, s4, 0x6a840000
	s_addc_u32 s25, s5, 0
	s_cmpk_lt_i32 s6, 0x4000
	s_cselect_b64 s[10:11], -1, 0
	v_readlane_b32 s8, v253, 1
	v_cndmask_b32_e64 v0, 0, 1, s[10:11]
	v_readlane_b32 s9, v253, 2
	s_mov_b64 s[2:3], -1
	s_and_b64 vcc, exec, s[14:15]
	v_cmp_ne_u32_e64 s[36:37], 1, v0
	v_readlane_b32 s17, v253, 9
	v_readlane_b32 s20, v253, 12
	v_readlane_b32 s21, v253, 13
	s_cbranch_vccz .LBB0_1323
	s_and_b64 vcc, exec, s[36:37]
	s_movk_i32 s27, 0x1000
	s_mov_b32 s30, 0xf800000
	s_mov_b32 s34, 0x4b800000
	s_cbranch_vccnz .LBB0_1322
	v_and_b32_e32 v0, 64, v215
	v_add_u32_e32 v0, 64, v0
	v_xor_b32_e32 v1, 1, v215
	v_cmp_lt_i32_e32 vcc, v1, v0
	s_load_dwordx2 s[2:3], s[8:9], 0xc8
	v_ashrrev_i32_e32 v17, 31, v16
	v_cndmask_b32_e32 v1, v215, v1, vcc
	v_lshlrev_b32_e32 v3, 2, v1
	v_xor_b32_e32 v1, 2, v215
	v_cmp_lt_i32_e32 vcc, v1, v0
	s_add_i32 s26, s6, 0xfffff000
	s_lshl_b32 s10, s6, 1
	v_cndmask_b32_e32 v1, v215, v1, vcc
	v_lshlrev_b32_e32 v27, 2, v1
	v_xor_b32_e32 v1, 4, v215
	v_cmp_lt_i32_e32 vcc, v1, v0
	v_readlane_b32 s40, v253, 8
	v_readlane_b32 s41, v253, 9
	v_cndmask_b32_e32 v1, v215, v1, vcc
	v_lshlrev_b32_e32 v77, 2, v1
	v_xor_b32_e32 v1, 8, v215
	v_cmp_lt_i32_e32 vcc, v1, v0
	v_lshl_add_u64 v[20:21], v[16:17], 2, s[0:1]
	v_lshlrev_b64 v[22:23], 3, v[16:17]
	v_cndmask_b32_e32 v1, v215, v1, vcc
	v_lshlrev_b32_e32 v80, 2, v1
	v_xor_b32_e32 v1, 16, v215
	v_cmp_lt_i32_e32 vcc, v1, v0
	v_readlane_b32 s42, v253, 10
	v_readlane_b32 s43, v253, 11
	v_cndmask_b32_e32 v1, v215, v1, vcc
	v_lshlrev_b32_e32 v81, 2, v1
	v_xor_b32_e32 v1, 32, v215
	v_cmp_lt_i32_e32 vcc, v1, v0
	v_readlane_b32 s44, v253, 12
	v_readlane_b32 s45, v253, 13
	v_cndmask_b32_e32 v0, v215, v1, vcc
	v_lshlrev_b32_e32 v82, 2, v0
	v_lshlrev_b64 v[0:1], 4, v[16:17]
	s_waitcnt lgkmcnt(0)
	v_lshl_add_u64 v[8:9], s[2:3], 0, v[0:1]
	s_mov_b64 s[2:3], 0x1000
	v_lshl_add_u64 v[10:11], v[8:9], 0, s[2:3]
	s_mov_b64 s[2:3], 0x1400
	v_lshl_add_u64 v[12:13], v[8:9], 0, s[2:3]
	s_mov_b64 s[2:3], 0x1800
	v_lshl_add_u64 v[14:15], v[8:9], 0, s[2:3]
	s_mov_b64 s[2:3], 0x1c00
	v_lshl_add_u64 v[18:19], v[8:9], 0, s[2:3]
	s_add_i32 s2, s6, 0x800
	s_ashr_i32 s3, s2, 31
	s_lshl_b64 s[12:13], s[2:3], 13
	s_add_u32 s12, s40, s12
	s_addc_u32 s13, s41, s13
	s_ashr_i32 s7, s6, 31
	s_lshl_b64 s[16:17], s[6:7], 12
	s_add_u32 s16, s4, s16
	s_addc_u32 s17, s5, s17
	s_lshl_b64 s[2:3], s[2:3], 12
	s_add_u32 s18, s4, s2
	s_addc_u32 s19, s5, s3
	s_lshl_b64 s[2:3], s[6:7], 13
	s_add_u32 s20, s40, s2
	s_addc_u32 s21, s41, s3
	v_readlane_b32 s46, v253, 14
	v_readlane_b32 s47, v253, 15
	global_load_dwordx4 v[160:163], v[8:9], off
	global_load_dwordx4 v[164:167], v[8:9], off offset:1024
	global_load_dwordx4 v[168:171], v[8:9], off offset:2048
	global_load_dwordx4 v[172:175], v[8:9], off offset:3072
	global_load_dwordx4 v[176:179], v[10:11], off
	global_load_dwordx4 v[180:183], v[12:13], off
	global_load_dwordx4 v[184:187], v[14:15], off
	global_load_dwordx4 v[188:191], v[18:19], off
	s_waitcnt vmcnt(0)
.LBB0_1321:
	s_ashr_i32 s11, s10, 31
	v_lshl_add_u64 v[4:5], s[16:17], 0, v[22:23]
	s_lshl_b64 s[2:3], s[10:11], 2
	v_add_co_u32_e32 v4, vcc, 0x4b800000, v4
	s_add_u32 s28, s24, s2
	s_nop 0
	v_addc_co_u32_e32 v5, vcc, 0, v5, vcc
	s_addc_u32 s29, s25, s3
	global_load_dwordx2 v[58:59], v[4:5], off
	global_load_dwordx2 v[52:53], v[4:5], off offset:512
	global_load_dwordx2 v[50:51], v[4:5], off offset:1024
	global_load_dwordx2 v[48:49], v[4:5], off offset:1536
	global_load_dwordx2 v[44:45], v[4:5], off offset:2048
	global_load_dwordx2 v[46:47], v[4:5], off offset:2560
	global_load_dwordx2 v[6:7], v[4:5], off offset:3072
	s_nop 0
	global_load_dwordx2 v[4:5], v[4:5], off offset:3584
	s_waitcnt vmcnt(7)
	v_lshlrev_b32_e32 v66, 16, v58
	global_load_dwordx2 v[24:25], v2, s[28:29]
	s_add_i32 s28, s10, 1
	s_ashr_i32 s29, s28, 31
	s_add_u32 s2, s22, s2
	s_addc_u32 s3, s23, s3
	v_and_b32_e32 v67, 0xffff0000, v58
	v_lshlrev_b32_e32 v58, 16, v59
	v_and_b32_e32 v59, 0xffff0000, v59
	s_waitcnt vmcnt(2)
	v_and_b32_e32 v99, 0xffff0000, v6
	s_waitcnt vmcnt(0)
	v_mul_f32_e32 v54, 0x3d800000, v24
	global_load_dword v24, v2, s[2:3]
	s_lshl_b64 s[2:3], s[28:29], 2
	s_add_u32 s2, s22, s2
	s_addc_u32 s3, s23, s3
	global_load_dword v28, v2, s[2:3]
	v_mul_f32_e32 v76, 0x3d800000, v25
	s_add_i32 s2, s10, 0x1000
	s_ashr_i32 s3, s2, 31
	s_lshl_b64 s[2:3], s[2:3], 2
	s_add_u32 s28, s24, s2
	s_addc_u32 s29, s25, s3
	s_waitcnt vmcnt(1)
	v_ashrrev_i32_e32 v25, 31, v24
	v_lshlrev_b64 v[24:25], 11, v[24:25]
	v_lshl_add_u64 v[24:25], v[20:21], 0, v[24:25]
	s_waitcnt vmcnt(0)
; #define GAS __attribute__((address_space(1)))
; template <int MODE, bool W8 = false>
; __device__ __forceinline__ void norm_rows(const Ctx& C, const void* src, bf16* xdst, const unsigned char* YS8, const int* srow, const float* gate, const float* gain, bf16* XN, float* outf, unsigned char* XN8 = nullptr) {
;     ...
;             if (MODE >= 1) {
;                 h0[q] = gate[2 * m] * (1.0f / SY); h1[q] = gate[2 * m + 1] * (1.0f / SY);
;                 const GAS unsigned* y0 = (const GAS unsigned*)(YS8 + (size_t)srow[2 * m] * DM) + C.lane; const GAS unsigned* y1 = (const GAS unsigned*)(YS8 + (size_t)srow[2 * m + 1] * DM) + C.lane;
; #pragma unroll
;                 for (int j = 0; j < 8; ++j) { ya[q][j] = y0[64 * j]; yb[q][j] = y1[64 * j]; } } }
; #pragma unroll
;         for (int q = 0; q < NR; ++q) { const int m = m0 + q * C.NGW;
;             if (MODE >= 1) {
; #pragma unroll
;                 for (int j = 0; j < 8; ++j) { const unsigned a = ya[q][j], b = yb[q][j];
;                     const f32x2_m a01 = __builtin_amdgcn_cvt_pk_f32_fp8((int)a, false), a23 = __builtin_amdgcn_cvt_pk_f32_fp8((int)a, true), b01 = __builtin_amdgcn_cvt_pk_f32_fp8((int)b, false), b23 = __builtin_amdgcn_cvt_pk_f32_fp8((int)b, true);
;                     v[q][j].x += h0[q] * a01.x + h1[q] * b01.x; v[q][j].y += h0[q] * a01.y + h1[q] * b01.y; v[q][j].z += h0[q] * a23.x + h1[q] * b23.x; v[q][j].w += h0[q] * a23.y + h1[q] * b23.y; } }
	v_ashrrev_i32_e32 v29, 31, v28
	v_lshlrev_b64 v[28:29], 11, v[28:29]
	v_lshl_add_u64 v[28:29], v[20:21], 0, v[28:29]
	global_load_dword v55, v[24:25], off
	global_load_dword v64, v[28:29], off
	global_load_dword v68, v[24:25], off offset:256
	global_load_dword v69, v[28:29], off offset:256
	global_load_dword v70, v[24:25], off offset:512
	global_load_dword v71, v[28:29], off offset:512
	global_load_dword v72, v[24:25], off offset:768
	global_load_dword v73, v[28:29], off offset:768
	global_load_dword v74, v[24:25], off offset:1024
	global_load_dword v75, v[28:29], off offset:1024
	global_load_dword v78, v[24:25], off offset:1280
	global_load_dword v79, v[28:29], off offset:1280
	global_load_dword v97, v[24:25], off offset:1536
	global_load_dword v98, v[28:29], off offset:1536
	global_load_dword v100, v[24:25], off offset:1792
	global_load_dword v101, v[28:29], off offset:1792
	v_lshl_add_u64 v[24:25], s[18:19], 0, v[22:23]
	v_add_co_u32_e32 v24, vcc, s34, v24
	s_waitcnt vmcnt(14)
	v_cvt_pk_f32_fp8_e32 v[62:63], v64
	v_addc_co_u32_e32 v25, vcc, 0, v25, vcc
	global_load_dwordx2 v[42:43], v[24:25], off
	global_load_dwordx2 v[40:41], v[24:25], off offset:512
	global_load_dwordx2 v[38:39], v[24:25], off offset:1024
	global_load_dwordx2 v[36:37], v[24:25], off offset:1536
	global_load_dwordx2 v[34:35], v[24:25], off offset:2048
	global_load_dwordx2 v[32:33], v[24:25], off offset:2560
	global_load_dwordx2 v[30:31], v[24:25], off offset:3072
	s_nop 0
	global_load_dwordx2 v[24:25], v[24:25], off offset:3584
	v_cvt_pk_f32_fp8_sdwa v[64:65], v64 src0_sel:WORD_1
	global_load_dwordx2 v[28:29], v2, s[28:29]
	s_add_i32 s28, s10, 0x1001
	s_ashr_i32 s29, s28, 31
	s_add_u32 s2, s22, s2
	s_addc_u32 s3, s23, s3
	global_load_dword v56, v2, s[2:3]
	s_lshl_b64 s[2:3], s[28:29], 2
	s_add_u32 s2, s22, s2
	s_addc_u32 s3, s23, s3
	global_load_dword v60, v2, s[2:3]
	v_pk_mul_f32 v[62:63], v[76:77], v[62:63] op_sel_hi:[0,1]
	s_addk_i32 s26, 0x1000
	s_addk_i32 s10, 0x2000
	s_waitcnt vmcnt(2)
	v_mul_f32_e32 v26, 0x3d800000, v28
	v_mul_f32_e32 v28, 0x3d800000, v29
	s_waitcnt vmcnt(1)
	v_ashrrev_i32_e32 v57, 31, v56
	v_lshlrev_b64 v[56:57], 11, v[56:57]
	v_lshl_add_u64 v[56:57], v[20:21], 0, v[56:57]
	s_waitcnt vmcnt(0)
	v_ashrrev_i32_e32 v61, 31, v60
	v_lshlrev_b64 v[60:61], 11, v[60:61]
	v_lshl_add_u64 v[60:61], v[20:21], 0, v[60:61]
	global_load_dword v96, v[56:57], off
	global_load_dword v95, v[60:61], off
	global_load_dword v94, v[56:57], off offset:256
	global_load_dword v93, v[60:61], off offset:256
	global_load_dword v92, v[56:57], off offset:512
	global_load_dword v91, v[60:61], off offset:512
	global_load_dword v90, v[56:57], off offset:768
	global_load_dword v89, v[60:61], off offset:768
	global_load_dword v88, v[56:57], off offset:1024
	global_load_dword v87, v[60:61], off offset:1024
	global_load_dword v86, v[56:57], off offset:1280
	global_load_dword v85, v[60:61], off offset:1280
	global_load_dword v84, v[56:57], off offset:1536
	global_load_dword v83, v[60:61], off offset:1536
	global_load_dword v29, v[56:57], off offset:1792
	global_load_dword v17, v[60:61], off offset:1792
	v_cvt_pk_f32_fp8_e32 v[56:57], v55
	v_cvt_pk_f32_fp8_sdwa v[60:61], v55 src0_sel:WORD_1
	v_pk_fma_f32 v[56:57], v[54:55], v[56:57], v[62:63] op_sel_hi:[0,1,1]
	v_pk_mul_f32 v[62:63], v[76:77], v[64:65] op_sel_hi:[0,1]
	v_pk_fma_f32 v[60:61], v[54:55], v[60:61], v[62:63] op_sel_hi:[0,1,1]
	v_cvt_pk_f32_fp8_e32 v[64:65], v69
	v_pk_add_f32 v[56:57], v[56:57], v[66:67]
	v_pk_add_f32 v[62:63], v[60:61], v[58:59]
	v_cvt_pk_f32_fp8_e32 v[58:59], v68
	v_cvt_pk_f32_fp8_sdwa v[66:67], v69 src0_sel:WORD_1
	v_cvt_pk_f32_fp8_sdwa v[60:61], v68 src0_sel:WORD_1
	v_pk_mul_f32 v[64:65], v[76:77], v[64:65] op_sel_hi:[0,1]
	v_pk_fma_f32 v[58:59], v[54:55], v[58:59], v[64:65] op_sel_hi:[0,1,1]
	v_pk_mul_f32 v[64:65], v[76:77], v[66:67] op_sel_hi:[0,1]
	v_lshlrev_b32_e32 v68, 16, v52
	v_and_b32_e32 v69, 0xffff0000, v52
	v_lshlrev_b32_e32 v52, 16, v53
	v_and_b32_e32 v53, 0xffff0000, v53
	v_pk_fma_f32 v[60:61], v[54:55], v[60:61], v[64:65] op_sel_hi:[0,1,1]
	v_pk_add_f32 v[66:67], v[60:61], v[52:53]
	v_cvt_pk_f32_fp8_e32 v[60:61], v71
	v_cvt_pk_f32_fp8_e32 v[52:53], v70
	v_pk_add_f32 v[58:59], v[58:59], v[68:69]
	v_cvt_pk_f32_fp8_sdwa v[68:69], v71 src0_sel:WORD_1
	v_cvt_pk_f32_fp8_sdwa v[64:65], v70 src0_sel:WORD_1
	v_pk_mul_f32 v[60:61], v[76:77], v[60:61] op_sel_hi:[0,1]
	v_lshlrev_b32_e32 v70, 16, v50
	v_and_b32_e32 v71, 0xffff0000, v50
	v_pk_fma_f32 v[52:53], v[54:55], v[52:53], v[60:61] op_sel_hi:[0,1,1]
	v_pk_add_f32 v[60:61], v[52:53], v[70:71]
	v_pk_mul_f32 v[52:53], v[76:77], v[68:69] op_sel_hi:[0,1]
	v_lshlrev_b32_e32 v50, 16, v51
	v_and_b32_e32 v51, 0xffff0000, v51
	v_pk_fma_f32 v[52:53], v[54:55], v[64:65], v[52:53] op_sel_hi:[0,1,1]
	v_cvt_pk_f32_fp8_e32 v[64:65], v73
	v_pk_add_f32 v[70:71], v[52:53], v[50:51]
	v_cvt_pk_f32_fp8_e32 v[50:51], v72
	v_cvt_pk_f32_fp8_sdwa v[68:69], v73 src0_sel:WORD_1
	v_cvt_pk_f32_fp8_sdwa v[52:53], v72 src0_sel:WORD_1
	v_pk_mul_f32 v[64:65], v[76:77], v[64:65] op_sel_hi:[0,1]
	v_lshlrev_b32_e32 v72, 16, v48
	v_and_b32_e32 v73, 0xffff0000, v48
	v_pk_fma_f32 v[50:51], v[54:55], v[50:51], v[64:65] op_sel_hi:[0,1,1]
	v_pk_add_f32 v[64:65], v[50:51], v[72:73]
	v_pk_mul_f32 v[50:51], v[76:77], v[68:69] op_sel_hi:[0,1]
	v_lshlrev_b32_e32 v48, 16, v49
	v_and_b32_e32 v49, 0xffff0000, v49
	v_pk_fma_f32 v[50:51], v[54:55], v[52:53], v[50:51] op_sel_hi:[0,1,1]
	v_cvt_pk_f32_fp8_e32 v[52:53], v75
	v_pk_add_f32 v[72:73], v[50:51], v[48:49]
	v_cvt_pk_f32_fp8_e32 v[48:49], v74
	v_cvt_pk_f32_fp8_sdwa v[50:51], v74 src0_sel:WORD_1
	v_cvt_pk_f32_fp8_sdwa v[74:75], v75 src0_sel:WORD_1
; template <int MODE, bool W8 = false>
; __device__ __forceinline__ void norm_rows(const Ctx& C, const void* src, bf16* xdst, const unsigned char* YS8, const int* srow, const float* gate, const float* gain, bf16* XN, float* outf, unsigned char* XN8 = nullptr) {
;     ...
;                 for (int j = 0; j < 8; ++j) { const unsigned a = ya[q][j], b = yb[q][j];
;                     const f32x2_m a01 = __builtin_amdgcn_cvt_pk_f32_fp8((int)a, false), a23 = __builtin_amdgcn_cvt_pk_f32_fp8((int)a, true), b01 = __builtin_amdgcn_cvt_pk_f32_fp8((int)b, false), b23 = __builtin_amdgcn_cvt_pk_f32_fp8((int)b, true);
;                     v[q][j].x += h0[q] * a01.x + h1[q] * b01.x; v[q][j].y += h0[q] * a01.y + h1[q] * b01.y; v[q][j].z += h0[q] * a23.x + h1[q] * b23.x; v[q][j].w += h0[q] * a23.y + h1[q] * b23.y; } }
;             float ss = 0.f;
; #pragma unroll
;             for (int j = 0; j < 8; ++j) ss += (v[q][j].x * v[q][j].x + v[q][j].y * v[q][j].y) + (v[q][j].z * v[q][j].z + v[q][j].w * v[q][j].w);
;             const float rstd = 1.0f / sqrtf(wave_sum(ss) * (1.0f / DM) + RMS_EPS);
	v_pk_mul_f32 v[52:53], v[76:77], v[52:53] op_sel_hi:[0,1]
	v_lshlrev_b32_e32 v68, 16, v44
	v_and_b32_e32 v69, 0xffff0000, v44
	v_pk_fma_f32 v[48:49], v[54:55], v[48:49], v[52:53] op_sel_hi:[0,1,1]
	v_pk_add_f32 v[68:69], v[48:49], v[68:69]
	v_pk_mul_f32 v[48:49], v[76:77], v[74:75] op_sel_hi:[0,1]
	v_lshlrev_b32_e32 v44, 16, v45
	v_and_b32_e32 v45, 0xffff0000, v45
	v_pk_fma_f32 v[48:49], v[54:55], v[50:51], v[48:49] op_sel_hi:[0,1,1]
	v_cvt_pk_f32_fp8_e32 v[50:51], v79
	v_pk_add_f32 v[74:75], v[48:49], v[44:45]
	v_cvt_pk_f32_fp8_e32 v[44:45], v78
	v_cvt_pk_f32_fp8_sdwa v[52:53], v79 src0_sel:WORD_1
	v_cvt_pk_f32_fp8_sdwa v[48:49], v78 src0_sel:WORD_1
	v_pk_mul_f32 v[50:51], v[76:77], v[50:51] op_sel_hi:[0,1]
	v_pk_fma_f32 v[44:45], v[54:55], v[44:45], v[50:51] op_sel_hi:[0,1,1]
	v_pk_mul_f32 v[50:51], v[76:77], v[52:53] op_sel_hi:[0,1]
	v_lshlrev_b32_e32 v78, 16, v46
	v_and_b32_e32 v79, 0xffff0000, v46
	v_lshlrev_b32_e32 v46, 16, v47
	v_and_b32_e32 v47, 0xffff0000, v47
	v_pk_fma_f32 v[48:49], v[54:55], v[48:49], v[50:51] op_sel_hi:[0,1,1]
	v_cvt_pk_f32_fp8_e32 v[52:53], v98
	v_pk_add_f32 v[44:45], v[44:45], v[78:79]
	v_pk_add_f32 v[46:47], v[48:49], v[46:47]
	v_cvt_pk_f32_fp8_e32 v[48:49], v97
	v_cvt_pk_f32_fp8_sdwa v[78:79], v98 src0_sel:WORD_1
	v_cvt_pk_f32_fp8_sdwa v[50:51], v97 src0_sel:WORD_1
	v_pk_mul_f32 v[52:53], v[76:77], v[52:53] op_sel_hi:[0,1]
	v_pk_fma_f32 v[48:49], v[54:55], v[48:49], v[52:53] op_sel_hi:[0,1,1]
	v_pk_mul_f32 v[52:53], v[76:77], v[78:79] op_sel_hi:[0,1]
	v_lshlrev_b32_e32 v98, 16, v6
	v_lshlrev_b32_e32 v6, 16, v7
	v_and_b32_e32 v7, 0xffff0000, v7
	v_pk_fma_f32 v[50:51], v[54:55], v[50:51], v[52:53] op_sel_hi:[0,1,1]
	v_cvt_pk_f32_fp8_e32 v[52:53], v101
	v_pk_add_f32 v[50:51], v[50:51], v[6:7]
	v_cvt_pk_f32_fp8_e32 v[6:7], v100
	v_pk_add_f32 v[48:49], v[48:49], v[98:99]
	v_cvt_pk_f32_fp8_sdwa v[98:99], v101 src0_sel:WORD_1
	v_cvt_pk_f32_fp8_sdwa v[78:79], v100 src0_sel:WORD_1
	v_pk_mul_f32 v[52:53], v[76:77], v[52:53] op_sel_hi:[0,1]
	v_lshlrev_b32_e32 v100, 16, v4
	v_and_b32_e32 v101, 0xffff0000, v4
	v_pk_fma_f32 v[6:7], v[54:55], v[6:7], v[52:53] op_sel_hi:[0,1,1]
	v_pk_add_f32 v[52:53], v[6:7], v[100:101]
	v_pk_mul_f32 v[6:7], v[76:77], v[98:99] op_sel_hi:[0,1]
	v_lshlrev_b32_e32 v4, 16, v5
	v_and_b32_e32 v5, 0xffff0000, v5
	v_pk_fma_f32 v[6:7], v[54:55], v[78:79], v[6:7] op_sel_hi:[0,1,1]
	v_pk_add_f32 v[54:55], v[6:7], v[4:5]
	v_mov_b32_e32 v6, v57
	v_mov_b32_e32 v7, v59
	v_mov_b32_e32 v4, v56
	v_mov_b32_e32 v5, v58
	v_pk_mul_f32 v[6:7], v[6:7], v[6:7]
	v_mov_b32_e32 v78, v63
	v_mov_b32_e32 v79, v67
	v_pk_fma_f32 v[4:5], v[4:5], v[4:5], v[6:7]
	v_mov_b32_e32 v6, v62
	v_mov_b32_e32 v7, v66
	v_pk_mul_f32 v[78:79], v[78:79], v[78:79]
	v_mul_f32_e32 v76, v65, v65
	v_pk_fma_f32 v[6:7], v[6:7], v[6:7], v[78:79]
	v_mov_b32_e32 v78, v61
	v_mov_b32_e32 v79, v71
	v_pk_add_f32 v[4:5], v[4:5], v[6:7]
	v_mov_b32_e32 v6, v60
	v_mov_b32_e32 v7, v70
	v_pk_mul_f32 v[78:79], v[78:79], v[78:79]
	v_pk_add_f32 v[4:5], v[4:5], v[4:5] op_sel:[0,1] op_sel_hi:[1,0]
	v_pk_fma_f32 v[6:7], v[6:7], v[6:7], v[78:79]
	v_pk_fma_f32 v[78:79], v[64:65], v[64:65], v[76:77] op_sel_hi:[1,1,0]
	v_mul_f32_e32 v76, v73, v73
	v_pk_add_f32 v[6:7], v[6:7], v[6:7] op_sel:[0,1] op_sel_hi:[1,0]
	v_pk_fma_f32 v[98:99], v[72:73], v[72:73], v[76:77] op_sel_hi:[1,1,0]
	v_pk_mul_f32 v[100:101], v[68:69], v[68:69]
	v_pk_mul_f32 v[102:103], v[74:75], v[74:75]
	v_mov_b32_e32 v5, v100
	v_mov_b32_e32 v7, v101
	v_mov_b32_e32 v79, v102
	v_mov_b32_e32 v99, v103
	v_pk_add_f32 v[4:5], v[4:5], v[6:7]
	v_pk_add_f32 v[6:7], v[78:79], v[98:99]
	v_mov_b32_e32 v78, v45
	v_mov_b32_e32 v79, v47
	v_pk_add_f32 v[4:5], v[4:5], v[6:7]
	v_mov_b32_e32 v6, v44
	v_mov_b32_e32 v7, v46
	v_pk_mul_f32 v[78:79], v[78:79], v[78:79]
	v_mul_f32_e32 v76, v49, v49
	v_pk_fma_f32 v[6:7], v[6:7], v[6:7], v[78:79]
	v_pk_fma_f32 v[78:79], v[48:49], v[48:49], v[76:77] op_sel_hi:[1,1,0]
	v_mul_f32_e32 v76, v51, v51
	v_pk_add_f32 v[4:5], v[4:5], v[4:5] op_sel:[0,1] op_sel_hi:[1,0]
	v_pk_add_f32 v[6:7], v[6:7], v[6:7] op_sel:[0,1] op_sel_hi:[1,0]
	v_pk_fma_f32 v[98:99], v[50:51], v[50:51], v[76:77] op_sel_hi:[1,1,0]
	v_pk_mul_f32 v[100:101], v[52:53], v[52:53]
	v_pk_mul_f32 v[102:103], v[54:55], v[54:55]
	v_mov_b32_e32 v5, v100
	v_mov_b32_e32 v7, v101
	v_mov_b32_e32 v79, v102
	v_mov_b32_e32 v99, v103
	v_pk_add_f32 v[4:5], v[4:5], v[6:7]
	v_pk_add_f32 v[6:7], v[78:79], v[98:99]
	s_nop 0
	v_pk_add_f32 v[4:5], v[4:5], v[6:7]
	s_nop 0
	v_add_f32_e32 v4, v4, v5
	ds_bpermute_b32 v5, v3, v4
	s_waitcnt lgkmcnt(0)
	v_add_f32_e32 v4, v4, v5
	ds_bpermute_b32 v5, v27, v4
	s_waitcnt lgkmcnt(0)
	v_add_f32_e32 v4, v4, v5
	ds_bpermute_b32 v5, v77, v4
	s_waitcnt lgkmcnt(0)
	v_add_f32_e32 v4, v4, v5
	ds_bpermute_b32 v5, v80, v4
	s_waitcnt lgkmcnt(0)
	v_add_f32_e32 v4, v4, v5
	ds_bpermute_b32 v5, v81, v4
	s_waitcnt lgkmcnt(0)
	v_add_f32_e32 v4, v4, v5
	ds_bpermute_b32 v5, v82, v4
	s_waitcnt lgkmcnt(0)
; #define GAS __attribute__((address_space(1)))
; __device__ __forceinline__ unsigned pk2(float lo, float hi) { f32x2_m v = {lo, hi}; bf16x2_m b = __builtin_convertvector(v, bf16x2_m); return __builtin_bit_cast(unsigned, b); }
; template <int MODE, bool W8 = false>
; __device__ __forceinline__ void norm_rows(const Ctx& C, const void* src, bf16* xdst, const unsigned char* YS8, const int* srow, const float* gate, const float* gain, bf16* XN, float* outf, unsigned char* XN8 = nullptr) {
;     ...
;             float ss = 0.f;
; #pragma unroll
;             for (int j = 0; j < 8; ++j) ss += (v[q][j].x * v[q][j].x + v[q][j].y * v[q][j].y) + (v[q][j].z * v[q][j].z + v[q][j].w * v[q][j].w);
;             const float rstd = 1.0f / sqrtf(wave_sum(ss) * (1.0f / DM) + RMS_EPS);
;             if (MODE == 1) { GAS v2u* xo = (GAS v2u*)(xdst + (size_t)m * DM) + C.lane;
; #pragma unroll
;                 for (int j = 0; j < 8; ++j) { v2u w; w.x = pk2(v[q][j].x, v[q][j].y); w.y = pk2(v[q][j].z, v[q][j].w); xo[64 * j] = w; } }
;             const GAS f32x4* gg = (const GAS f32x4*)gain + C.lane;
;             if (MODE <= 1) { GAS v2u* o = (GAS v2u*)(XN + (size_t)m * DM) + C.lane;
; #pragma unroll
;                 for (int j = 0; j < 8; ++j) { const f32x4 g = gg[64 * j]; const f32x4 y = v[q][j] * rstd * g; v2u w; w.x = pk2(y.x, y.y); w.y = pk2(y.z, y.w); o[64 * j] = w;
;                     if constexpr (W8) ((GAS unsigned*)(XN8 + (size_t)m * DM) + C.lane)[64 * j] = pk4_fp8m(y.x * SXN, y.y * SXN, y.z * SXN, y.w * SXN); } }
;             else { GAS f32x4* o = (GAS f32x4*)(outf + (size_t)m * DM) + C.lane;
; #pragma unroll
;                 for (int j = 0; j < 8; ++j) { const f32x4 g = gg[64 * j]; o[64 * j] = v[q][j] * rstd * g; } } }
	v_add_f32_e32 v4, v4, v5
	v_fmamk_f32 v4, v4, 0x3a000000, v212
	v_cmp_gt_f32_e32 vcc, s30, v4
	v_mul_f32_e32 v5, 0x4f800000, v4
	s_nop 0
	v_cndmask_b32_e32 v4, v4, v5, vcc
	v_sqrt_f32_e32 v5, v4
	s_nop 0
	v_add_u32_e32 v6, -1, v5
	v_fma_f32 v7, -v6, v5, v4
	v_cmp_ge_f32_e64 s[2:3], 0, v7
	v_add_u32_e32 v7, 1, v5
	s_nop 0
	v_cndmask_b32_e64 v6, v5, v6, s[2:3]
	v_fma_f32 v5, -v7, v5, v4
	v_cmp_lt_f32_e64 s[2:3], 0, v5
	s_nop 1
	v_cndmask_b32_e64 v5, v6, v7, s[2:3]
	v_mul_f32_e32 v6, 0x37800000, v5
	v_cndmask_b32_e32 v5, v5, v6, vcc
	v_cmp_class_f32_e32 vcc, v4, v211
	s_nop 1
	v_cndmask_b32_e32 v4, v5, v4, vcc
	v_div_scale_f32 v5, s[2:3], v4, v4, 1.0
	v_rcp_f32_e32 v6, v5
	s_nop 0
	v_fma_f32 v7, -v5, v6, 1.0
	v_fmac_f32_e32 v6, v7, v6
	v_div_scale_f32 v7, vcc, 1.0, v4, 1.0
	v_mul_f32_e32 v76, v7, v6
	v_fma_f32 v78, -v5, v76, v7
	v_fmac_f32_e32 v76, v78, v6
	v_fma_f32 v5, -v5, v76, v7
	v_div_fmas_f32 v5, v5, v6, v76
	v_div_fixup_f32 v76, v5, v4, 1.0
	v_pk_mul_f32 v[56:57], v[56:57], v[76:77] op_sel_hi:[1,0]
	v_pk_mul_f32 v[62:63], v[62:63], v[76:77] op_sel_hi:[1,0]
	v_lshl_add_u64 v[78:79], s[20:21], 0, v[0:1]
	v_pk_mul_f32 v[58:59], v[58:59], v[76:77] op_sel_hi:[1,0]
	v_pk_mul_f32 v[46:47], v[46:47], v[76:77] op_sel_hi:[1,0]
	v_pk_mul_f32 v[44:45], v[44:45], v[76:77] op_sel_hi:[1,0]
	v_pk_mul_f32 v[6:7], v[162:163], v[62:63]
	v_pk_mul_f32 v[4:5], v[160:161], v[56:57]
	global_store_dwordx4 v[78:79], v[4:7], off
	s_nop 1
	v_pk_mul_f32 v[56:57], v[66:67], v[76:77] op_sel_hi:[1,0]
	v_lshlrev_b32_e32 v62, 16, v24
	v_and_b32_e32 v63, 0xffff0000, v24
	v_lshlrev_b32_e32 v24, 16, v25
	v_and_b32_e32 v25, 0xffff0000, v25
	v_pk_mul_f32 v[4:5], v[164:165], v[58:59]
	v_pk_mul_f32 v[6:7], v[166:167], v[56:57]
	global_store_dwordx4 v[78:79], v[4:7], off offset:1024
	s_nop 1
	v_pk_mul_f32 v[56:57], v[70:71], v[76:77] op_sel_hi:[1,0]
	v_pk_mul_f32 v[58:59], v[60:61], v[76:77] op_sel_hi:[1,0]
	v_lshlrev_b32_e32 v60, 16, v30
	v_and_b32_e32 v61, 0xffff0000, v30
	v_lshlrev_b32_e32 v30, 16, v31
	v_and_b32_e32 v31, 0xffff0000, v31
	v_pk_mul_f32 v[4:5], v[168:169], v[58:59]
	v_pk_mul_f32 v[6:7], v[170:171], v[56:57]
	global_store_dwordx4 v[78:79], v[4:7], off offset:2048
	s_nop 1
	v_pk_mul_f32 v[56:57], v[72:73], v[76:77] op_sel_hi:[1,0]
	v_pk_mul_f32 v[58:59], v[64:65], v[76:77] op_sel_hi:[1,0]
	v_pk_mul_f32 v[6:7], v[174:175], v[56:57]
	v_pk_mul_f32 v[4:5], v[172:173], v[58:59]
	global_store_dwordx4 v[78:79], v[4:7], off offset:3072
	s_nop 1
	v_pk_mul_f32 v[56:57], v[74:75], v[76:77] op_sel_hi:[1,0]
	v_pk_mul_f32 v[58:59], v[68:69], v[76:77] op_sel_hi:[1,0]
	v_pk_mul_f32 v[6:7], v[178:179], v[56:57]
	v_add_co_u32_e32 v56, vcc, s27, v78
	v_pk_mul_f32 v[4:5], v[176:177], v[58:59]
	s_nop 0
	v_addc_co_u32_e32 v57, vcc, 0, v79, vcc
	global_store_dwordx4 v[56:57], v[4:7], off
	s_nop 1
	v_lshlrev_b32_e32 v58, 16, v32
	v_and_b32_e32 v59, 0xffff0000, v32
	v_lshlrev_b32_e32 v32, 16, v33
	v_and_b32_e32 v33, 0xffff0000, v33
	v_pk_mul_f32 v[4:5], v[180:181], v[44:45]
	v_pk_mul_f32 v[6:7], v[182:183], v[46:47]
	global_store_dwordx4 v[56:57], v[4:7], off offset:1024
	s_nop 1
	v_pk_mul_f32 v[44:45], v[50:51], v[76:77] op_sel_hi:[1,0]
	v_pk_mul_f32 v[46:47], v[48:49], v[76:77] op_sel_hi:[1,0]
	v_lshlrev_b32_e32 v48, 16, v42
	v_and_b32_e32 v49, 0xffff0000, v42
	v_lshlrev_b32_e32 v50, 16, v40
	v_and_b32_e32 v51, 0xffff0000, v40
	v_pk_mul_f32 v[4:5], v[184:185], v[46:47]
	v_pk_mul_f32 v[6:7], v[186:187], v[44:45]
	global_store_dwordx4 v[56:57], v[4:7], off offset:2048
	s_nop 1
	v_pk_mul_f32 v[44:45], v[54:55], v[76:77] op_sel_hi:[1,0]
	v_pk_mul_f32 v[46:47], v[52:53], v[76:77] op_sel_hi:[1,0]
	v_lshlrev_b32_e32 v52, 16, v38
	v_and_b32_e32 v53, 0xffff0000, v38
	v_lshlrev_b32_e32 v54, 16, v36
	v_and_b32_e32 v55, 0xffff0000, v36
	v_pk_mul_f32 v[4:5], v[188:189], v[46:47]
	v_pk_mul_f32 v[6:7], v[190:191], v[44:45]
	s_waitcnt vmcnt(7)
	v_cvt_pk_f32_fp8_e32 v[44:45], v95
	global_store_dwordx4 v[56:57], v[4:7], off offset:3072
	s_nop 1
	v_cvt_pk_f32_fp8_sdwa v[46:47], v95 src0_sel:WORD_1
	v_lshlrev_b32_e32 v56, 16, v34
	v_cvt_pk_f32_fp8_e32 v[4:5], v96
	v_cvt_pk_f32_fp8_sdwa v[6:7], v96 src0_sel:WORD_1
	v_pk_mul_f32 v[44:45], v[28:29], v[44:45] op_sel_hi:[0,1]
	v_and_b32_e32 v57, 0xffff0000, v34
	v_pk_fma_f32 v[4:5], v[26:27], v[4:5], v[44:45] op_sel_hi:[0,1,1]
	v_pk_add_f32 v[44:45], v[4:5], v[48:49]
	v_lshlrev_b32_e32 v4, 16, v43
	v_and_b32_e32 v5, 0xffff0000, v43
	v_pk_mul_f32 v[42:43], v[28:29], v[46:47] op_sel_hi:[0,1]
	v_pk_fma_f32 v[6:7], v[26:27], v[6:7], v[42:43] op_sel_hi:[0,1,1]
	v_cvt_pk_f32_fp8_e32 v[42:43], v93
	v_pk_add_f32 v[46:47], v[6:7], v[4:5]
	v_cvt_pk_f32_fp8_e32 v[4:5], v94
	v_cvt_pk_f32_fp8_sdwa v[48:49], v93 src0_sel:WORD_1
	v_cvt_pk_f32_fp8_sdwa v[6:7], v94 src0_sel:WORD_1
	v_pk_mul_f32 v[42:43], v[28:29], v[42:43] op_sel_hi:[0,1]
	v_pk_fma_f32 v[4:5], v[26:27], v[4:5], v[42:43] op_sel_hi:[0,1,1]
	v_pk_add_f32 v[42:43], v[4:5], v[50:51]
	v_lshlrev_b32_e32 v4, 16, v41
	v_and_b32_e32 v5, 0xffff0000, v41
	v_pk_mul_f32 v[40:41], v[28:29], v[48:49] op_sel_hi:[0,1]
	v_pk_fma_f32 v[6:7], v[26:27], v[6:7], v[40:41] op_sel_hi:[0,1,1]
	v_cvt_pk_f32_fp8_e32 v[40:41], v91
	v_pk_add_f32 v[48:49], v[6:7], v[4:5]
	v_cvt_pk_f32_fp8_e32 v[4:5], v92
	v_cvt_pk_f32_fp8_sdwa v[50:51], v91 src0_sel:WORD_1
	v_cvt_pk_f32_fp8_sdwa v[6:7], v92 src0_sel:WORD_1
	v_pk_mul_f32 v[40:41], v[28:29], v[40:41] op_sel_hi:[0,1]
	v_pk_fma_f32 v[4:5], v[26:27], v[4:5], v[40:41] op_sel_hi:[0,1,1]
	v_pk_add_f32 v[40:41], v[4:5], v[52:53]
	v_lshlrev_b32_e32 v4, 16, v39
	v_and_b32_e32 v5, 0xffff0000, v39
	v_pk_mul_f32 v[38:39], v[28:29], v[50:51] op_sel_hi:[0,1]
	v_pk_fma_f32 v[6:7], v[26:27], v[6:7], v[38:39] op_sel_hi:[0,1,1]
; template <int MODE, bool W8 = false>
; __device__ __forceinline__ void norm_rows(const Ctx& C, const void* src, bf16* xdst, const unsigned char* YS8, const int* srow, const float* gate, const float* gain, bf16* XN, float* outf, unsigned char* XN8 = nullptr) {
;     ...
;             if (MODE >= 1) {
; #pragma unroll
;                 for (int j = 0; j < 8; ++j) { const unsigned a = ya[q][j], b = yb[q][j];
;                     const f32x2_m a01 = __builtin_amdgcn_cvt_pk_f32_fp8((int)a, false), a23 = __builtin_amdgcn_cvt_pk_f32_fp8((int)a, true), b01 = __builtin_amdgcn_cvt_pk_f32_fp8((int)b, false), b23 = __builtin_amdgcn_cvt_pk_f32_fp8((int)b, true);
;                     v[q][j].x += h0[q] * a01.x + h1[q] * b01.x; v[q][j].y += h0[q] * a01.y + h1[q] * b01.y; v[q][j].z += h0[q] * a23.x + h1[q] * b23.x; v[q][j].w += h0[q] * a23.y + h1[q] * b23.y; } }
;             float ss = 0.f;
; #pragma unroll
;             for (int j = 0; j < 8; ++j) ss += (v[q][j].x * v[q][j].x + v[q][j].y * v[q][j].y) + (v[q][j].z * v[q][j].z + v[q][j].w * v[q][j].w);
	v_cvt_pk_f32_fp8_e32 v[38:39], v89
	v_pk_add_f32 v[50:51], v[6:7], v[4:5]
	v_cvt_pk_f32_fp8_e32 v[4:5], v90
	v_cvt_pk_f32_fp8_sdwa v[52:53], v89 src0_sel:WORD_1
	v_cvt_pk_f32_fp8_sdwa v[6:7], v90 src0_sel:WORD_1
	v_pk_mul_f32 v[38:39], v[28:29], v[38:39] op_sel_hi:[0,1]
	v_pk_fma_f32 v[4:5], v[26:27], v[4:5], v[38:39] op_sel_hi:[0,1,1]
	v_pk_add_f32 v[38:39], v[4:5], v[54:55]
	v_lshlrev_b32_e32 v4, 16, v37
	v_and_b32_e32 v5, 0xffff0000, v37
	v_pk_mul_f32 v[36:37], v[28:29], v[52:53] op_sel_hi:[0,1]
	v_pk_fma_f32 v[6:7], v[26:27], v[6:7], v[36:37] op_sel_hi:[0,1,1]
	v_cvt_pk_f32_fp8_e32 v[36:37], v87
	v_pk_add_f32 v[52:53], v[6:7], v[4:5]
	v_cvt_pk_f32_fp8_e32 v[4:5], v88
	v_cvt_pk_f32_fp8_sdwa v[54:55], v87 src0_sel:WORD_1
	v_cvt_pk_f32_fp8_sdwa v[6:7], v88 src0_sel:WORD_1
	v_pk_mul_f32 v[36:37], v[28:29], v[36:37] op_sel_hi:[0,1]
	v_pk_fma_f32 v[4:5], v[26:27], v[4:5], v[36:37] op_sel_hi:[0,1,1]
	v_pk_add_f32 v[36:37], v[4:5], v[56:57]
	v_lshlrev_b32_e32 v4, 16, v35
	v_and_b32_e32 v5, 0xffff0000, v35
	v_pk_mul_f32 v[34:35], v[28:29], v[54:55] op_sel_hi:[0,1]
	v_pk_fma_f32 v[6:7], v[26:27], v[6:7], v[34:35] op_sel_hi:[0,1,1]
	v_cvt_pk_f32_fp8_e32 v[34:35], v85
	v_pk_add_f32 v[54:55], v[6:7], v[4:5]
	v_cvt_pk_f32_fp8_e32 v[4:5], v86
	v_cvt_pk_f32_fp8_sdwa v[56:57], v85 src0_sel:WORD_1
	v_cvt_pk_f32_fp8_sdwa v[6:7], v86 src0_sel:WORD_1
	v_pk_mul_f32 v[34:35], v[28:29], v[34:35] op_sel_hi:[0,1]
	v_pk_fma_f32 v[4:5], v[26:27], v[4:5], v[34:35] op_sel_hi:[0,1,1]
	v_pk_mul_f32 v[34:35], v[28:29], v[56:57] op_sel_hi:[0,1]
	v_pk_fma_f32 v[6:7], v[26:27], v[6:7], v[34:35] op_sel_hi:[0,1,1]
	v_cvt_pk_f32_fp8_e32 v[56:57], v83
	v_pk_add_f32 v[32:33], v[6:7], v[32:33]
	v_cvt_pk_f32_fp8_e32 v[6:7], v84
	v_pk_add_f32 v[4:5], v[4:5], v[58:59]
	v_cvt_pk_f32_fp8_sdwa v[58:59], v83 src0_sel:WORD_1
	v_cvt_pk_f32_fp8_sdwa v[34:35], v84 src0_sel:WORD_1
	v_pk_mul_f32 v[56:57], v[28:29], v[56:57] op_sel_hi:[0,1]
	v_pk_fma_f32 v[6:7], v[26:27], v[6:7], v[56:57] op_sel_hi:[0,1,1]
	v_pk_add_f32 v[6:7], v[6:7], v[60:61]
	v_pk_mul_f32 v[56:57], v[28:29], v[58:59] op_sel_hi:[0,1]
	v_cvt_pk_f32_fp8_e32 v[58:59], v17
	v_cvt_pk_f32_fp8_sdwa v[60:61], v17 src0_sel:WORD_1
	v_pk_fma_f32 v[34:35], v[26:27], v[34:35], v[56:57] op_sel_hi:[0,1,1]
	v_cvt_pk_f32_fp8_sdwa v[56:57], v29 src0_sel:WORD_1
	v_pk_add_f32 v[34:35], v[34:35], v[30:31]
	v_cvt_pk_f32_fp8_e32 v[30:31], v29
	v_pk_mul_f32 v[58:59], v[28:29], v[58:59] op_sel_hi:[0,1]
	v_pk_mul_f32 v[28:29], v[28:29], v[60:61] op_sel_hi:[0,1]
	v_pk_fma_f32 v[28:29], v[26:27], v[56:57], v[28:29] op_sel_hi:[0,1,1]
	v_mov_b32_e32 v56, v45
	v_mov_b32_e32 v57, v43
	v_pk_fma_f32 v[30:31], v[26:27], v[30:31], v[58:59] op_sel_hi:[0,1,1]
	v_pk_add_f32 v[24:25], v[28:29], v[24:25]
	v_mov_b32_e32 v28, v44
	v_mov_b32_e32 v29, v42
	v_pk_mul_f32 v[56:57], v[56:57], v[56:57]
	v_mov_b32_e32 v58, v47
	v_mov_b32_e32 v59, v49
	v_pk_fma_f32 v[28:29], v[28:29], v[28:29], v[56:57]
	v_mov_b32_e32 v56, v46
	v_mov_b32_e32 v57, v48
	v_pk_mul_f32 v[58:59], v[58:59], v[58:59]
	v_mul_f32_e32 v26, v39, v39
	v_pk_fma_f32 v[56:57], v[56:57], v[56:57], v[58:59]
	v_mov_b32_e32 v58, v41
	v_mov_b32_e32 v59, v51
	v_pk_add_f32 v[28:29], v[28:29], v[56:57]
	v_mov_b32_e32 v56, v40
	v_mov_b32_e32 v57, v50
	v_pk_mul_f32 v[58:59], v[58:59], v[58:59]
	v_pk_add_f32 v[30:31], v[30:31], v[62:63]
	v_pk_fma_f32 v[56:57], v[56:57], v[56:57], v[58:59]
	v_pk_fma_f32 v[58:59], v[38:39], v[38:39], v[26:27] op_sel_hi:[1,1,0]
	v_mul_f32_e32 v26, v53, v53
	v_pk_add_f32 v[28:29], v[28:29], v[28:29] op_sel:[0,1] op_sel_hi:[1,0]
	v_pk_add_f32 v[56:57], v[56:57], v[56:57] op_sel:[0,1] op_sel_hi:[1,0]
	v_pk_fma_f32 v[60:61], v[52:53], v[52:53], v[26:27] op_sel_hi:[1,1,0]
	v_pk_mul_f32 v[62:63], v[36:37], v[36:37]
	v_pk_mul_f32 v[64:65], v[54:55], v[54:55]
	v_mov_b32_e32 v29, v62
	v_mov_b32_e32 v57, v63
	v_mov_b32_e32 v59, v64
	v_mov_b32_e32 v61, v65
	v_pk_add_f32 v[28:29], v[28:29], v[56:57]
	v_pk_add_f32 v[56:57], v[58:59], v[60:61]
	v_mov_b32_e32 v58, v5
	v_mov_b32_e32 v59, v33
	v_pk_add_f32 v[28:29], v[28:29], v[56:57]
	v_mov_b32_e32 v56, v4
	v_mov_b32_e32 v57, v32
	v_pk_mul_f32 v[58:59], v[58:59], v[58:59]
	v_mul_f32_e32 v26, v7, v7
	v_pk_fma_f32 v[56:57], v[56:57], v[56:57], v[58:59]
	v_pk_fma_f32 v[58:59], v[6:7], v[6:7], v[26:27] op_sel_hi:[1,1,0]
	v_mul_f32_e32 v26, v35, v35
	v_pk_add_f32 v[28:29], v[28:29], v[28:29] op_sel:[0,1] op_sel_hi:[1,0]
	v_pk_add_f32 v[56:57], v[56:57], v[56:57] op_sel:[0,1] op_sel_hi:[1,0]
	v_pk_fma_f32 v[60:61], v[34:35], v[34:35], v[26:27] op_sel_hi:[1,1,0]
	v_pk_mul_f32 v[62:63], v[30:31], v[30:31]
	v_pk_mul_f32 v[64:65], v[24:25], v[24:25]
	v_mov_b32_e32 v29, v62
	v_mov_b32_e32 v57, v63
	v_mov_b32_e32 v59, v64
	v_mov_b32_e32 v61, v65
	v_pk_add_f32 v[28:29], v[28:29], v[56:57]
	v_pk_add_f32 v[56:57], v[58:59], v[60:61]
	s_nop 0
	v_pk_add_f32 v[28:29], v[28:29], v[56:57]
	s_nop 0
	v_add_f32_e32 v17, v28, v29
	ds_bpermute_b32 v26, v3, v17
	s_waitcnt lgkmcnt(0)
; #define GAS __attribute__((address_space(1)))
; __device__ __forceinline__ unsigned pk2(float lo, float hi) { f32x2_m v = {lo, hi}; bf16x2_m b = __builtin_convertvector(v, bf16x2_m); return __builtin_bit_cast(unsigned, b); }
; template <int MODE, bool W8 = false>
; __device__ __forceinline__ void norm_rows(const Ctx& C, const void* src, bf16* xdst, const unsigned char* YS8, const int* srow, const float* gate, const float* gain, bf16* XN, float* outf, unsigned char* XN8 = nullptr) {
;     ...
;             float ss = 0.f;
; #pragma unroll
;             for (int j = 0; j < 8; ++j) ss += (v[q][j].x * v[q][j].x + v[q][j].y * v[q][j].y) + (v[q][j].z * v[q][j].z + v[q][j].w * v[q][j].w);
;             const float rstd = 1.0f / sqrtf(wave_sum(ss) * (1.0f / DM) + RMS_EPS);
;             if (MODE == 1) { GAS v2u* xo = (GAS v2u*)(xdst + (size_t)m * DM) + C.lane;
; #pragma unroll
;                 for (int j = 0; j < 8; ++j) { v2u w; w.x = pk2(v[q][j].x, v[q][j].y); w.y = pk2(v[q][j].z, v[q][j].w); xo[64 * j] = w; } }
;             const GAS f32x4* gg = (const GAS f32x4*)gain + C.lane;
;             if (MODE <= 1) { GAS v2u* o = (GAS v2u*)(XN + (size_t)m * DM) + C.lane;
; #pragma unroll
;                 for (int j = 0; j < 8; ++j) { const f32x4 g = gg[64 * j]; const f32x4 y = v[q][j] * rstd * g; v2u w; w.x = pk2(y.x, y.y); w.y = pk2(y.z, y.w); o[64 * j] = w;
;                     if constexpr (W8) ((GAS unsigned*)(XN8 + (size_t)m * DM) + C.lane)[64 * j] = pk4_fp8m(y.x * SXN, y.y * SXN, y.z * SXN, y.w * SXN); } }
;             else { GAS f32x4* o = (GAS f32x4*)(outf + (size_t)m * DM) + C.lane;
; #pragma unroll
;                 for (int j = 0; j < 8; ++j) { const f32x4 g = gg[64 * j]; o[64 * j] = v[q][j] * rstd * g; } } }
	v_add_f32_e32 v17, v17, v26
	ds_bpermute_b32 v26, v27, v17
	s_waitcnt lgkmcnt(0)
	v_add_f32_e32 v17, v17, v26
	ds_bpermute_b32 v26, v77, v17
	s_waitcnt lgkmcnt(0)
	v_add_f32_e32 v17, v17, v26
	ds_bpermute_b32 v26, v80, v17
	s_waitcnt lgkmcnt(0)
	v_add_f32_e32 v17, v17, v26
	ds_bpermute_b32 v26, v81, v17
	s_waitcnt lgkmcnt(0)
	v_add_f32_e32 v17, v17, v26
	ds_bpermute_b32 v26, v82, v17
	s_waitcnt lgkmcnt(0)
	v_add_f32_e32 v17, v17, v26
	v_fmamk_f32 v17, v17, 0x3a000000, v212
	v_cmp_gt_f32_e32 vcc, s30, v17
	v_mul_f32_e32 v26, 0x4f800000, v17
	s_nop 0
	v_cndmask_b32_e32 v17, v17, v26, vcc
	v_sqrt_f32_e32 v26, v17
	s_nop 0
	v_add_u32_e32 v28, -1, v26
	v_fma_f32 v29, -v28, v26, v17
	v_cmp_ge_f32_e64 s[2:3], 0, v29
	v_add_u32_e32 v29, 1, v26
	s_nop 0
	v_cndmask_b32_e64 v28, v26, v28, s[2:3]
	v_fma_f32 v26, -v29, v26, v17
	v_cmp_lt_f32_e64 s[2:3], 0, v26
	s_nop 1
	v_cndmask_b32_e64 v26, v28, v29, s[2:3]
	v_mul_f32_e32 v28, 0x37800000, v26
	v_cndmask_b32_e32 v26, v26, v28, vcc
	v_cmp_class_f32_e32 vcc, v17, v211
	s_nop 1
	v_cndmask_b32_e32 v17, v26, v17, vcc
	v_div_scale_f32 v26, s[2:3], v17, v17, 1.0
	v_rcp_f32_e32 v28, v26
	s_nop 0
	v_fma_f32 v29, -v26, v28, 1.0
	v_fmac_f32_e32 v28, v29, v28
	v_div_scale_f32 v29, vcc, 1.0, v17, 1.0
	v_mul_f32_e32 v56, v29, v28
	v_fma_f32 v57, -v26, v56, v29
	v_fmac_f32_e32 v56, v57, v28
	v_fma_f32 v26, -v26, v56, v29
	v_div_fmas_f32 v26, v26, v28, v56
	v_div_fixup_f32 v26, v26, v17, 1.0
	v_pk_mul_f32 v[46:47], v[46:47], v[26:27] op_sel_hi:[1,0]
	v_pk_mul_f32 v[44:45], v[44:45], v[26:27] op_sel_hi:[1,0]
	v_lshl_add_u64 v[28:29], s[12:13], 0, v[0:1]
	v_pk_mul_f32 v[48:49], v[48:49], v[26:27] op_sel_hi:[1,0]
	v_pk_mul_f32 v[42:43], v[42:43], v[26:27] op_sel_hi:[1,0]
	v_pk_mul_f32 v[40:41], v[40:41], v[26:27] op_sel_hi:[1,0]
	v_pk_mul_f32 v[38:39], v[38:39], v[26:27] op_sel_hi:[1,0]
	v_pk_mul_f32 v[36:37], v[36:37], v[26:27] op_sel_hi:[1,0]
	v_pk_mul_f32 v[32:33], v[32:33], v[26:27] op_sel_hi:[1,0]
	v_pk_mul_f32 v[4:5], v[4:5], v[26:27] op_sel_hi:[1,0]
	s_add_u32 s12, s12, 0x2000000
	s_addc_u32 s13, s13, 0
	s_add_u32 s16, s16, 0x1000000
	s_addc_u32 s17, s17, 0
	s_add_u32 s18, s18, 0x1000000
	s_addc_u32 s19, s19, 0
	s_add_u32 s20, s20, 0x2000000
	v_pk_mul_f32 v[24:25], v[24:25], v[26:27] op_sel_hi:[1,0]
	v_pk_mul_f32 v[30:31], v[30:31], v[26:27] op_sel_hi:[1,0]
	s_addc_u32 s21, s21, 0
	s_cmpk_lt_i32 s26, 0x3000
	v_pk_mul_f32 v[44:45], v[160:161], v[44:45]
	v_pk_mul_f32 v[46:47], v[162:163], v[46:47]
	global_store_dwordx4 v[28:29], v[44:47], off
	s_nop 1
	v_pk_mul_f32 v[42:43], v[164:165], v[42:43]
	v_pk_mul_f32 v[44:45], v[166:167], v[48:49]
	global_store_dwordx4 v[28:29], v[42:45], off offset:1024
	s_nop 1
	v_pk_mul_f32 v[46:47], v[50:51], v[26:27] op_sel_hi:[1,0]
	v_pk_mul_f32 v[40:41], v[168:169], v[40:41]
	v_pk_mul_f32 v[42:43], v[170:171], v[46:47]
	global_store_dwordx4 v[28:29], v[40:43], off offset:2048
	s_nop 1
	v_pk_mul_f32 v[44:45], v[52:53], v[26:27] op_sel_hi:[1,0]
	v_pk_mul_f32 v[38:39], v[172:173], v[38:39]
	v_pk_mul_f32 v[40:41], v[174:175], v[44:45]
	global_store_dwordx4 v[28:29], v[38:41], off offset:3072
	s_nop 1
	v_pk_mul_f32 v[42:43], v[54:55], v[26:27] op_sel_hi:[1,0]
	v_add_co_u32_e32 v28, vcc, s27, v28
	v_pk_mul_f32 v[36:37], v[176:177], v[36:37]
	v_pk_mul_f32 v[38:39], v[178:179], v[42:43]
	v_addc_co_u32_e32 v29, vcc, 0, v29, vcc
	global_store_dwordx4 v[28:29], v[36:39], off
	s_nop 1
	v_pk_mul_f32 v[36:37], v[180:181], v[4:5]
	v_pk_mul_f32 v[38:39], v[182:183], v[32:33]
	global_store_dwordx4 v[28:29], v[36:39], off offset:1024
	s_nop 1
	v_pk_mul_f32 v[32:33], v[34:35], v[26:27] op_sel_hi:[1,0]
	v_pk_mul_f32 v[4:5], v[6:7], v[26:27] op_sel_hi:[1,0]
	v_pk_mul_f32 v[6:7], v[186:187], v[32:33]
	v_pk_mul_f32 v[4:5], v[184:185], v[4:5]
	global_store_dwordx4 v[28:29], v[4:7], off offset:2048
	s_nop 1
	v_pk_mul_f32 v[4:5], v[188:189], v[30:31]
	v_pk_mul_f32 v[6:7], v[190:191], v[24:25]
	global_store_dwordx4 v[28:29], v[4:7], off offset:3072
	s_nop 1
	s_cbranch_scc1 .LBB0_1321

; #define GAS __attribute__((address_space(1)))
; __device__ __forceinline__ float bflo(unsigned w) { return __uint_as_float(w << 16); }
; __device__ __forceinline__ float bfhi(unsigned w) { return __uint_as_float(w & 0xffff0000u); }
; template <int MODE, bool W8 = false>
; __device__ __forceinline__ void norm_rows(const Ctx& C, const void* src, bf16* xdst, const unsigned char* YS8, const int* srow, const float* gate, const float* gain, bf16* XN, float* outf, unsigned char* XN8 = nullptr) {
;     ...
;     for (int m0 = C.gw; m0 < T; m0 += NR * C.NGW) {
;         f32x4 v[NR][8]; unsigned ya[NR][8], yb[NR][8]; float h0[NR], h1[NR];
; #pragma unroll
;         for (int q = 0; q < NR; ++q) { const int m = m0 + q * C.NGW;
;             if (MODE == 0) { const GAS f32x4* xr = (const GAS f32x4*)((const float*)src + (size_t)m * DM) + C.lane;
; #pragma unroll
;                 for (int j = 0; j < 8; ++j) v[q][j] = xr[64 * j]; }
;             else { const GAS v2u* xr = (const GAS v2u*)((const bf16*)src + (size_t)m * DM) + C.lane;
; #pragma unroll
;                 for (int j = 0; j < 8; ++j) { const v2u t_ = xr[64 * j]; v[q][j] = (f32x4){bflo(t_.x), bfhi(t_.x), bflo(t_.y), bfhi(t_.y)}; } }
;             if (MODE >= 1) {
;                 h0[q] = gate[2 * m] * (1.0f / SY); h1[q] = gate[2 * m + 1] * (1.0f / SY);
;                 const GAS unsigned* y0 = (const GAS unsigned*)(YS8 + (size_t)srow[2 * m] * DM) + C.lane; const GAS unsigned* y1 = (const GAS unsigned*)(YS8 + (size_t)srow[2 * m + 1] * DM) + C.lane;
; #pragma unroll
;                 for (int j = 0; j < 8; ++j) { ya[q][j] = y0[64 * j]; yb[q][j] = y1[64 * j]; } } }
;     ...
;             const GAS f32x4* gg = (const GAS f32x4*)gain + C.lane;
.LBB0_1323:
	s_andn2_b64 vcc, exec, s[2:3]
	s_mov_b32 s12, 0xf800000
	s_mov_b32 s13, 0x4b800000
	s_brev_b32 s16, 44
	s_mov_b32 s17, 0x49800000
	s_mov_b64 s[18:19], 0x800000
	s_mov_b64 s[20:21], 0x1000000
	s_cbranch_vccnz .LBB0_1327
	s_and_b64 vcc, exec, s[36:37]
	s_cbranch_vccnz .LBB0_1327
	v_and_b32_e32 v0, 64, v215
	v_add_u32_e32 v0, 64, v0
	v_xor_b32_e32 v1, 1, v215
	v_cmp_lt_i32_e32 vcc, v1, v0
	s_load_dwordx2 s[2:3], s[8:9], 0x10
	v_ashrrev_i32_e32 v17, 31, v16
	v_cndmask_b32_e32 v1, v215, v1, vcc
	v_lshlrev_b32_e32 v3, 2, v1
	v_xor_b32_e32 v1, 2, v215
	v_cmp_lt_i32_e32 vcc, v1, v0
	v_lshlrev_b64 v[18:19], 2, v[16:17]
	s_waitcnt lgkmcnt(0)
	v_lshl_add_u64 v[12:13], v[16:17], 4, s[2:3]
	v_cndmask_b32_e32 v1, v215, v1, vcc
	v_lshlrev_b32_e32 v57, 2, v1
	v_xor_b32_e32 v1, 4, v215
	v_cmp_lt_i32_e32 vcc, v1, v0
	s_add_i32 s2, s6, 0x800
	s_ashr_i32 s3, s2, 31
	v_cndmask_b32_e32 v1, v215, v1, vcc
	v_lshlrev_b32_e32 v81, 2, v1
	v_xor_b32_e32 v1, 8, v215
	v_cmp_lt_i32_e32 vcc, v1, v0
	s_lshl_b64 s[10:11], s[2:3], 11
	s_lshl_b64 s[2:3], s[2:3], 12
	v_cndmask_b32_e32 v1, v215, v1, vcc
	v_lshlrev_b32_e32 v82, 2, v1
	v_xor_b32_e32 v1, 16, v215
	v_cmp_lt_i32_e32 vcc, v1, v0
	v_lshlrev_b64 v[20:21], 3, v[16:17]
	s_ashr_i32 s7, s6, 31
	v_cndmask_b32_e32 v1, v215, v1, vcc
	v_lshlrev_b32_e32 v83, 2, v1
	v_xor_b32_e32 v1, 32, v215
	v_cmp_lt_i32_e32 vcc, v1, v0
	v_lshl_add_u64 v[16:17], s[2:3], 0, v[20:21]
	s_lshl_b64 s[2:3], s[6:7], 11
	v_cndmask_b32_e32 v0, v215, v1, vcc
	v_lshlrev_b32_e32 v84, 2, v0
	v_lshl_add_u64 v[0:1], s[0:1], 0, v[18:19]
	s_mov_b64 s[0:1], 0x2000
	v_lshl_add_u64 v[4:5], v[12:13], 0, s[0:1]
	s_mov_b64 s[0:1], 0x3000
	v_lshl_add_u64 v[6:7], v[12:13], 0, s[0:1]
	s_mov_b64 s[0:1], 0x3400
	v_lshl_add_u64 v[8:9], v[12:13], 0, s[0:1]
	s_mov_b64 s[0:1], 0x3800
	v_lshl_add_u64 v[10:11], v[12:13], 0, s[0:1]
	s_mov_b64 s[0:1], 0x3c00
	v_lshl_add_u64 v[14:15], s[10:11], 0, v[18:19]
	v_lshl_add_u64 v[18:19], s[2:3], 0, v[18:19]
	s_lshl_b64 s[2:3], s[6:7], 12
	v_lshl_add_u64 v[12:13], v[12:13], 0, s[0:1]
	s_add_i32 s8, s6, 0xfffff000
	s_lshl_b32 s0, s6, 1
	v_lshl_add_u64 v[20:21], s[2:3], 0, v[20:21]
	global_load_dwordx4 v[160:163], v[4:5], off
	global_load_dwordx4 v[164:167], v[4:5], off offset:1024
	global_load_dwordx4 v[168:171], v[4:5], off offset:2048
	global_load_dwordx4 v[172:175], v[4:5], off offset:3072
	global_load_dwordx4 v[176:179], v[6:7], off
	global_load_dwordx4 v[180:183], v[8:9], off
	global_load_dwordx4 v[184:187], v[10:11], off
	global_load_dwordx4 v[188:191], v[12:13], off
	s_waitcnt vmcnt(0)
.LBB0_1326:
	s_ashr_i32 s1, s0, 31
	v_lshl_add_u64 v[52:53], s[4:5], 0, v[20:21]
	s_lshl_b64 s[2:3], s[0:1], 2
	v_add_co_u32_e32 v50, vcc, 0x4b800000, v52
	s_add_u32 s6, s24, s2
	s_nop 0
	v_addc_co_u32_e32 v51, vcc, 0, v53, vcc
	s_addc_u32 s7, s25, s3
	global_load_dwordx2 v[64:65], v[50:51], off
	global_load_dwordx2 v[62:63], v[50:51], off offset:512
	global_load_dwordx2 v[60:61], v[50:51], off offset:1024
	global_load_dwordx2 v[58:59], v[50:51], off offset:1536
	global_load_dwordx2 v[48:49], v[50:51], off offset:2048
	global_load_dwordx2 v[46:47], v[50:51], off offset:2560
	global_load_dwordx2 v[42:43], v[50:51], off offset:3072
	global_load_dwordx2 v[44:45], v[50:51], off offset:3584
	global_load_dwordx2 v[22:23], v2, s[6:7]
	s_add_i32 s6, s0, 1
	s_ashr_i32 s7, s6, 31
	s_add_u32 s2, s22, s2
	s_addc_u32 s3, s23, s3
	v_lshl_add_u64 v[28:29], s[4:5], 0, v[16:17]
	v_add_co_u32_e32 v26, vcc, s13, v28
	v_lshl_add_u64 v[16:17], v[16:17], 0, s[20:21]
	s_nop 0
	v_addc_co_u32_e32 v27, vcc, 0, v29, vcc
	v_lshl_add_u64 v[20:21], v[20:21], 0, s[20:21]
	s_waitcnt vmcnt(8)
	v_lshlrev_b32_e32 v74, 16, v64
	v_and_b32_e32 v75, 0xffff0000, v64
	v_lshlrev_b32_e32 v64, 16, v65
	v_and_b32_e32 v65, 0xffff0000, v65
	s_waitcnt vmcnt(0)
	v_mul_f32_e32 v78, 0x3d800000, v22
	global_load_dword v22, v2, s[2:3]
	s_lshl_b64 s[2:3], s[6:7], 2
	s_add_u32 s2, s22, s2
	s_addc_u32 s3, s23, s3
	global_load_dword v24, v2, s[2:3]
	s_add_i32 s2, s0, 0x1000
	s_ashr_i32 s3, s2, 31
	v_mul_f32_e32 v80, 0x3d800000, v23
	s_lshl_b64 s[2:3], s[2:3], 2
	s_add_u32 s6, s24, s2
	s_addc_u32 s7, s25, s3
	s_waitcnt vmcnt(1)
	v_ashrrev_i32_e32 v23, 31, v22
	v_lshlrev_b64 v[22:23], 11, v[22:23]
	v_lshl_add_u64 v[22:23], v[0:1], 0, v[22:23]
	s_waitcnt vmcnt(0)
	v_ashrrev_i32_e32 v25, 31, v24
	v_lshlrev_b64 v[24:25], 11, v[24:25]
	v_lshl_add_u64 v[24:25], v[0:1], 0, v[24:25]
	global_load_dword v70, v[22:23], off
	global_load_dword v72, v[24:25], off
	global_load_dword v76, v[22:23], off offset:256
	global_load_dword v77, v[24:25], off offset:256
	global_load_dword v79, v[22:23], off offset:512
	global_load_dword v100, v[24:25], off offset:512
	global_load_dword v101, v[22:23], off offset:768
	global_load_dword v102, v[24:25], off offset:768
	global_load_dword v103, v[22:23], off offset:1024
	global_load_dword v108, v[24:25], off offset:1024
	global_load_dword v109, v[22:23], off offset:1280
	global_load_dword v110, v[24:25], off offset:1280
	global_load_dword v111, v[22:23], off offset:1536
	global_load_dword v112, v[24:25], off offset:1536
	global_load_dword v113, v[22:23], off offset:1792
	global_load_dword v114, v[24:25], off offset:1792
	global_load_dwordx2 v[40:41], v[26:27], off
	global_load_dwordx2 v[38:39], v[26:27], off offset:512
	global_load_dwordx2 v[36:37], v[26:27], off offset:1024
	global_load_dwordx2 v[34:35], v[26:27], off offset:1536
	global_load_dwordx2 v[32:33], v[26:27], off offset:2048
	global_load_dwordx2 v[30:31], v[26:27], off offset:2560
	global_load_dwordx2 v[22:23], v[26:27], off offset:3072
	global_load_dwordx2 v[24:25], v[26:27], off offset:3584
	global_load_dwordx2 v[54:55], v2, s[6:7]
	s_add_i32 s6, s0, 0x1001
	s_ashr_i32 s7, s6, 31
	s_add_u32 s2, s22, s2
	s_addc_u32 s3, s23, s3
	global_load_dword v66, v2, s[2:3]
	s_lshl_b64 s[2:3], s[6:7], 2
	s_add_u32 s2, s22, s2
	s_addc_u32 s3, s23, s3
	global_load_dword v68, v2, s[2:3]
	s_addk_i32 s8, 0x1000
	s_addk_i32 s0, 0x2000
	s_cmpk_gt_i32 s8, 0x2fff
	s_waitcnt vmcnt(2)
; #define GAS __attribute__((address_space(1)))
; template <int MODE, bool W8 = false>
; __device__ __forceinline__ void norm_rows(const Ctx& C, const void* src, bf16* xdst, const unsigned char* YS8, const int* srow, const float* gate, const float* gain, bf16* XN, float* outf, unsigned char* XN8 = nullptr) {
;     ...
;             if (MODE >= 1) {
;                 h0[q] = gate[2 * m] * (1.0f / SY); h1[q] = gate[2 * m + 1] * (1.0f / SY);
;                 const GAS unsigned* y0 = (const GAS unsigned*)(YS8 + (size_t)srow[2 * m] * DM) + C.lane; const GAS unsigned* y1 = (const GAS unsigned*)(YS8 + (size_t)srow[2 * m + 1] * DM) + C.lane;
; #pragma unroll
;                 for (int j = 0; j < 8; ++j) { ya[q][j] = y0[64 * j]; yb[q][j] = y1[64 * j]; } } }
; #pragma unroll
;         for (int q = 0; q < NR; ++q) { const int m = m0 + q * C.NGW;
;             if (MODE >= 1) {
; #pragma unroll
;                 for (int j = 0; j < 8; ++j) { const unsigned a = ya[q][j], b = yb[q][j];
;                     const f32x2_m a01 = __builtin_amdgcn_cvt_pk_f32_fp8((int)a, false), a23 = __builtin_amdgcn_cvt_pk_f32_fp8((int)a, true), b01 = __builtin_amdgcn_cvt_pk_f32_fp8((int)b, false), b23 = __builtin_amdgcn_cvt_pk_f32_fp8((int)b, true);
;                     v[q][j].x += h0[q] * a01.x + h1[q] * b01.x; v[q][j].y += h0[q] * a01.y + h1[q] * b01.y; v[q][j].z += h0[q] * a23.x + h1[q] * b23.x; v[q][j].w += h0[q] * a23.y + h1[q] * b23.y; } }
	v_mul_f32_e32 v56, 0x3d800000, v55
	v_mul_f32_e32 v54, 0x3d800000, v54
	s_waitcnt vmcnt(1)
	v_ashrrev_i32_e32 v67, 31, v66
	v_lshlrev_b64 v[66:67], 11, v[66:67]
	v_lshl_add_u64 v[66:67], v[0:1], 0, v[66:67]
	s_waitcnt vmcnt(0)
	v_ashrrev_i32_e32 v69, 31, v68
	v_lshlrev_b64 v[68:69], 11, v[68:69]
	v_lshl_add_u64 v[68:69], v[0:1], 0, v[68:69]
	global_load_dword v99, v[66:67], off
	global_load_dword v98, v[68:69], off
	global_load_dword v97, v[66:67], off offset:256
	global_load_dword v96, v[68:69], off offset:256
	global_load_dword v95, v[66:67], off offset:512
	global_load_dword v94, v[68:69], off offset:512
	global_load_dword v93, v[66:67], off offset:768
	global_load_dword v92, v[68:69], off offset:768
	global_load_dword v91, v[66:67], off offset:1024
	global_load_dword v90, v[68:69], off offset:1024
	global_load_dword v89, v[66:67], off offset:1280
	global_load_dword v88, v[68:69], off offset:1280
	global_load_dword v87, v[66:67], off offset:1536
	global_load_dword v86, v[68:69], off offset:1536
	global_load_dword v85, v[66:67], off offset:1792
	global_load_dword v55, v[68:69], off offset:1792
	v_cvt_pk_f32_fp8_e32 v[66:67], v70
	v_cvt_pk_f32_fp8_sdwa v[68:69], v70 src0_sel:WORD_1
	v_cvt_pk_f32_fp8_e32 v[70:71], v72
	v_cvt_pk_f32_fp8_sdwa v[72:73], v72 src0_sel:WORD_1
	v_pk_mul_f32 v[70:71], v[80:81], v[70:71] op_sel_hi:[0,1]
	v_pk_fma_f32 v[66:67], v[78:79], v[66:67], v[70:71] op_sel_hi:[0,1,1]
	v_pk_add_f32 v[104:105], v[66:67], v[74:75]
	v_pk_mul_f32 v[66:67], v[80:81], v[72:73] op_sel_hi:[0,1]
	v_pk_fma_f32 v[66:67], v[78:79], v[68:69], v[66:67] op_sel_hi:[0,1,1]
	v_cvt_pk_f32_fp8_e32 v[68:69], v77
	v_pk_add_f32 v[106:107], v[66:67], v[64:65]
	v_cvt_pk_f32_fp8_e32 v[64:65], v76
	v_cvt_pk_f32_fp8_sdwa v[70:71], v77 src0_sel:WORD_1
	v_cvt_pk_f32_fp8_sdwa v[66:67], v76 src0_sel:WORD_1
	v_pk_mul_f32 v[68:69], v[80:81], v[68:69] op_sel_hi:[0,1]
	v_lshlrev_b32_e32 v72, 16, v62
	v_and_b32_e32 v73, 0xffff0000, v62
	v_pk_fma_f32 v[64:65], v[78:79], v[64:65], v[68:69] op_sel_hi:[0,1,1]
	v_pk_add_f32 v[74:75], v[64:65], v[72:73]
	v_pk_mul_f32 v[64:65], v[80:81], v[70:71] op_sel_hi:[0,1]
	v_lshlrev_b32_e32 v62, 16, v63
	v_and_b32_e32 v63, 0xffff0000, v63
	v_pk_fma_f32 v[64:65], v[78:79], v[66:67], v[64:65] op_sel_hi:[0,1,1]
	v_cvt_pk_f32_fp8_e32 v[66:67], v100
	v_pk_add_f32 v[76:77], v[64:65], v[62:63]
	v_cvt_pk_f32_fp8_e32 v[62:63], v79
	v_cvt_pk_f32_fp8_sdwa v[68:69], v100 src0_sel:WORD_1
	v_cvt_pk_f32_fp8_sdwa v[64:65], v79 src0_sel:WORD_1
	v_pk_mul_f32 v[66:67], v[80:81], v[66:67] op_sel_hi:[0,1]
	v_lshlrev_b32_e32 v70, 16, v60
	v_and_b32_e32 v71, 0xffff0000, v60
	v_pk_fma_f32 v[62:63], v[78:79], v[62:63], v[66:67] op_sel_hi:[0,1,1]
	v_pk_add_f32 v[70:71], v[62:63], v[70:71]
	v_pk_mul_f32 v[62:63], v[80:81], v[68:69] op_sel_hi:[0,1]
	v_lshlrev_b32_e32 v60, 16, v61
	v_and_b32_e32 v61, 0xffff0000, v61
	v_pk_fma_f32 v[62:63], v[78:79], v[64:65], v[62:63] op_sel_hi:[0,1,1]
	v_cvt_pk_f32_fp8_e32 v[64:65], v102
	v_pk_add_f32 v[72:73], v[62:63], v[60:61]
	v_cvt_pk_f32_fp8_e32 v[60:61], v101
	v_cvt_pk_f32_fp8_sdwa v[68:69], v102 src0_sel:WORD_1
	v_cvt_pk_f32_fp8_sdwa v[62:63], v101 src0_sel:WORD_1
	v_pk_mul_f32 v[64:65], v[80:81], v[64:65] op_sel_hi:[0,1]
	v_lshlrev_b32_e32 v66, 16, v58
	v_and_b32_e32 v67, 0xffff0000, v58
	v_pk_fma_f32 v[60:61], v[78:79], v[60:61], v[64:65] op_sel_hi:[0,1,1]
	v_pk_add_f32 v[66:67], v[60:61], v[66:67]
	v_pk_mul_f32 v[60:61], v[80:81], v[68:69] op_sel_hi:[0,1]
	v_lshlrev_b32_e32 v58, 16, v59
	v_and_b32_e32 v59, 0xffff0000, v59
	v_pk_fma_f32 v[60:61], v[78:79], v[62:63], v[60:61] op_sel_hi:[0,1,1]
	v_cvt_pk_f32_fp8_e32 v[62:63], v108
	v_pk_add_f32 v[68:69], v[60:61], v[58:59]
	v_cvt_pk_f32_fp8_e32 v[58:59], v103
	v_cvt_pk_f32_fp8_sdwa v[64:65], v108 src0_sel:WORD_1
	v_cvt_pk_f32_fp8_sdwa v[60:61], v103 src0_sel:WORD_1
	v_pk_mul_f32 v[62:63], v[80:81], v[62:63] op_sel_hi:[0,1]
	v_lshlrev_b32_e32 v100, 16, v48
	v_and_b32_e32 v101, 0xffff0000, v48
	v_pk_fma_f32 v[58:59], v[78:79], v[58:59], v[62:63] op_sel_hi:[0,1,1]
	v_pk_add_f32 v[62:63], v[58:59], v[100:101]
	v_pk_mul_f32 v[58:59], v[80:81], v[64:65] op_sel_hi:[0,1]
	v_lshlrev_b32_e32 v48, 16, v49
	v_and_b32_e32 v49, 0xffff0000, v49
	v_pk_fma_f32 v[58:59], v[78:79], v[60:61], v[58:59] op_sel_hi:[0,1,1]
	v_pk_add_f32 v[64:65], v[58:59], v[48:49]
	v_cvt_pk_f32_fp8_e32 v[58:59], v110
	v_cvt_pk_f32_fp8_e32 v[48:49], v109
	v_cvt_pk_f32_fp8_sdwa v[100:101], v110 src0_sel:WORD_1
	v_cvt_pk_f32_fp8_sdwa v[60:61], v109 src0_sel:WORD_1
	v_pk_mul_f32 v[58:59], v[80:81], v[58:59] op_sel_hi:[0,1]
	v_lshlrev_b32_e32 v102, 16, v46
	v_and_b32_e32 v103, 0xffff0000, v46
	v_pk_fma_f32 v[48:49], v[78:79], v[48:49], v[58:59] op_sel_hi:[0,1,1]
	v_pk_add_f32 v[58:59], v[48:49], v[102:103]
	v_pk_mul_f32 v[48:49], v[80:81], v[100:101] op_sel_hi:[0,1]
	v_lshlrev_b32_e32 v46, 16, v47
	v_and_b32_e32 v47, 0xffff0000, v47
	v_pk_fma_f32 v[48:49], v[78:79], v[60:61], v[48:49] op_sel_hi:[0,1,1]
	v_cvt_pk_f32_fp8_e32 v[100:101], v112
	v_pk_add_f32 v[60:61], v[48:49], v[46:47]
	v_cvt_pk_f32_fp8_e32 v[46:47], v111
	v_cvt_pk_f32_fp8_sdwa v[102:103], v112 src0_sel:WORD_1
	v_cvt_pk_f32_fp8_sdwa v[48:49], v111 src0_sel:WORD_1
	v_pk_mul_f32 v[100:101], v[80:81], v[100:101] op_sel_hi:[0,1]
	v_pk_fma_f32 v[46:47], v[78:79], v[46:47], v[100:101] op_sel_hi:[0,1,1]
	v_pk_mul_f32 v[100:101], v[80:81], v[102:103] op_sel_hi:[0,1]
	v_lshlrev_b32_e32 v108, 16, v42
	v_and_b32_e32 v109, 0xffff0000, v42
	v_lshlrev_b32_e32 v42, 16, v43
	v_and_b32_e32 v43, 0xffff0000, v43
	v_pk_fma_f32 v[48:49], v[78:79], v[48:49], v[100:101] op_sel_hi:[0,1,1]
	v_cvt_pk_f32_fp8_e32 v[102:103], v114
	v_pk_add_f32 v[46:47], v[46:47], v[108:109]
; #define GAS __attribute__((address_space(1)))
; __device__ __forceinline__ unsigned pk2(float lo, float hi) { f32x2_m v = {lo, hi}; bf16x2_m b = __builtin_convertvector(v, bf16x2_m); return __builtin_bit_cast(unsigned, b); }
; template <int MODE, bool W8 = false>
; __device__ __forceinline__ void norm_rows(const Ctx& C, const void* src, bf16* xdst, const unsigned char* YS8, const int* srow, const float* gate, const float* gain, bf16* XN, float* outf, unsigned char* XN8 = nullptr) {
;     ...
;             float ss = 0.f;
; #pragma unroll
;             for (int j = 0; j < 8; ++j) ss += (v[q][j].x * v[q][j].x + v[q][j].y * v[q][j].y) + (v[q][j].z * v[q][j].z + v[q][j].w * v[q][j].w);
;             const float rstd = 1.0f / sqrtf(wave_sum(ss) * (1.0f / DM) + RMS_EPS);
;             if (MODE == 1) { GAS v2u* xo = (GAS v2u*)(xdst + (size_t)m * DM) + C.lane;
; #pragma unroll
;                 for (int j = 0; j < 8; ++j) { v2u w; w.x = pk2(v[q][j].x, v[q][j].y); w.y = pk2(v[q][j].z, v[q][j].w); xo[64 * j] = w; } }
	v_pk_add_f32 v[48:49], v[48:49], v[42:43]
	v_cvt_pk_f32_fp8_e32 v[42:43], v113
	v_cvt_pk_f32_fp8_sdwa v[108:109], v114 src0_sel:WORD_1
	v_cvt_pk_f32_fp8_sdwa v[100:101], v113 src0_sel:WORD_1
	v_pk_mul_f32 v[102:103], v[80:81], v[102:103] op_sel_hi:[0,1]
	v_pk_fma_f32 v[42:43], v[78:79], v[42:43], v[102:103] op_sel_hi:[0,1,1]
	v_pk_mul_f32 v[102:103], v[80:81], v[108:109] op_sel_hi:[0,1]
	v_lshlrev_b32_e32 v110, 16, v44
	v_and_b32_e32 v111, 0xffff0000, v44
	v_lshlrev_b32_e32 v44, 16, v45
	v_and_b32_e32 v45, 0xffff0000, v45
	v_pk_fma_f32 v[78:79], v[78:79], v[100:101], v[102:103] op_sel_hi:[0,1,1]
	v_mov_b32_e32 v100, v105
	v_mov_b32_e32 v101, v75
	v_pk_add_f32 v[44:45], v[78:79], v[44:45]
	v_mov_b32_e32 v78, v104
	v_mov_b32_e32 v79, v74
	v_pk_mul_f32 v[100:101], v[100:101], v[100:101]
	v_mov_b32_e32 v102, v107
	v_mov_b32_e32 v103, v77
	v_pk_fma_f32 v[78:79], v[78:79], v[78:79], v[100:101]
	v_mov_b32_e32 v100, v106
	v_mov_b32_e32 v101, v76
	v_pk_mul_f32 v[102:103], v[102:103], v[102:103]
	v_mul_f32_e32 v80, v67, v67
	v_pk_fma_f32 v[100:101], v[100:101], v[100:101], v[102:103]
	v_mov_b32_e32 v102, v71
	v_mov_b32_e32 v103, v73
	v_pk_add_f32 v[78:79], v[78:79], v[100:101]
	v_mov_b32_e32 v100, v70
	v_mov_b32_e32 v101, v72
	v_pk_mul_f32 v[102:103], v[102:103], v[102:103]
	v_pk_add_f32 v[42:43], v[42:43], v[110:111]
	v_pk_fma_f32 v[100:101], v[100:101], v[100:101], v[102:103]
	v_pk_fma_f32 v[102:103], v[66:67], v[66:67], v[80:81] op_sel_hi:[1,1,0]
	v_mul_f32_e32 v80, v69, v69
	v_pk_add_f32 v[78:79], v[78:79], v[78:79] op_sel:[0,1] op_sel_hi:[1,0]
	v_pk_add_f32 v[100:101], v[100:101], v[100:101] op_sel:[0,1] op_sel_hi:[1,0]
	v_pk_fma_f32 v[108:109], v[68:69], v[68:69], v[80:81] op_sel_hi:[1,1,0]
	v_pk_mul_f32 v[110:111], v[62:63], v[62:63]
	v_pk_mul_f32 v[112:113], v[64:65], v[64:65]
	v_mov_b32_e32 v79, v110
	v_mov_b32_e32 v101, v111
	v_mov_b32_e32 v103, v112
	v_mov_b32_e32 v109, v113
	v_pk_add_f32 v[78:79], v[78:79], v[100:101]
	v_pk_add_f32 v[100:101], v[102:103], v[108:109]
	v_mov_b32_e32 v102, v59
	v_mov_b32_e32 v103, v61
	v_pk_add_f32 v[78:79], v[78:79], v[100:101]
	v_mov_b32_e32 v100, v58
	v_mov_b32_e32 v101, v60
	v_pk_mul_f32 v[102:103], v[102:103], v[102:103]
	v_mul_f32_e32 v80, v47, v47
	v_pk_fma_f32 v[100:101], v[100:101], v[100:101], v[102:103]
	v_pk_fma_f32 v[102:103], v[46:47], v[46:47], v[80:81] op_sel_hi:[1,1,0]
	v_mul_f32_e32 v80, v49, v49
	v_pk_add_f32 v[78:79], v[78:79], v[78:79] op_sel:[0,1] op_sel_hi:[1,0]
	v_pk_add_f32 v[100:101], v[100:101], v[100:101] op_sel:[0,1] op_sel_hi:[1,0]
	v_pk_fma_f32 v[108:109], v[48:49], v[48:49], v[80:81] op_sel_hi:[1,1,0]
	v_pk_mul_f32 v[110:111], v[42:43], v[42:43]
	v_pk_mul_f32 v[112:113], v[44:45], v[44:45]
	v_mov_b32_e32 v79, v110
	v_mov_b32_e32 v101, v111
	v_mov_b32_e32 v103, v112
	v_mov_b32_e32 v109, v113
	v_pk_add_f32 v[78:79], v[78:79], v[100:101]
	v_pk_add_f32 v[100:101], v[102:103], v[108:109]
	s_nop 0
	v_pk_add_f32 v[78:79], v[78:79], v[100:101]
	s_nop 0
	v_add_f32_e32 v78, v78, v79
	ds_bpermute_b32 v79, v3, v78
	s_waitcnt lgkmcnt(0)
	v_add_f32_e32 v78, v78, v79
	ds_bpermute_b32 v79, v57, v78
	s_waitcnt lgkmcnt(0)
	v_add_f32_e32 v78, v78, v79
	ds_bpermute_b32 v79, v81, v78
	s_waitcnt lgkmcnt(0)
	v_add_f32_e32 v78, v78, v79
	ds_bpermute_b32 v79, v82, v78
	s_waitcnt lgkmcnt(0)
	v_add_f32_e32 v78, v78, v79
	ds_bpermute_b32 v79, v83, v78
	s_waitcnt lgkmcnt(0)
	v_add_f32_e32 v78, v78, v79
	ds_bpermute_b32 v79, v84, v78
	s_waitcnt lgkmcnt(0)
	v_add_f32_e32 v78, v78, v79
	v_fmamk_f32 v78, v78, 0x3a000000, v212
	v_cmp_gt_f32_e32 vcc, s12, v78
	v_mul_f32_e32 v79, 0x4f800000, v78
	s_nop 0
	v_cndmask_b32_e32 v78, v78, v79, vcc
	v_sqrt_f32_e32 v79, v78
	s_nop 0
	v_add_u32_e32 v80, -1, v79
	v_fma_f32 v100, -v80, v79, v78
	v_cmp_ge_f32_e64 s[2:3], 0, v100
	v_add_u32_e32 v100, 1, v79
	s_nop 0
	v_cndmask_b32_e64 v80, v79, v80, s[2:3]
	v_fma_f32 v79, -v100, v79, v78
	v_cmp_lt_f32_e64 s[2:3], 0, v79
	s_nop 1
	v_cndmask_b32_e64 v79, v80, v100, s[2:3]
	v_mul_f32_e32 v80, 0x37800000, v79
	v_cndmask_b32_e32 v79, v79, v80, vcc
	v_cmp_class_f32_e32 vcc, v78, v211
	s_nop 1
	v_cndmask_b32_e32 v80, v79, v78, vcc
	v_cvt_pk_bf16_f32 v78, v104, v105
	v_cvt_pk_bf16_f32 v79, v106, v107
	global_store_dwordx2 v[50:51], v[78:79], off
	s_nop 1
	v_cvt_pk_bf16_f32 v78, v74, v75
	v_cvt_pk_bf16_f32 v79, v76, v77
	global_store_dwordx2 v[50:51], v[78:79], off offset:512
	s_nop 1
	v_cvt_pk_bf16_f32 v78, v70, v71
	v_cvt_pk_bf16_f32 v79, v72, v73
	global_store_dwordx2 v[50:51], v[78:79], off offset:1024
	s_nop 1
	v_cvt_pk_bf16_f32 v78, v66, v67
	v_cvt_pk_bf16_f32 v79, v68, v69
	global_store_dwordx2 v[50:51], v[78:79], off offset:1536
	s_nop 1
	v_cvt_pk_bf16_f32 v78, v62, v63
	v_cvt_pk_bf16_f32 v79, v64, v65
	global_store_dwordx2 v[50:51], v[78:79], off offset:2048
	s_nop 1
	v_cvt_pk_bf16_f32 v78, v58, v59
	v_cvt_pk_bf16_f32 v79, v60, v61
	global_store_dwordx2 v[50:51], v[78:79], off offset:2560
	s_nop 1
	v_cvt_pk_bf16_f32 v78, v46, v47
	v_cvt_pk_bf16_f32 v79, v48, v49
	global_store_dwordx2 v[50:51], v[78:79], off offset:3072
	s_nop 1
	v_cvt_pk_bf16_f32 v78, v42, v43
	v_cvt_pk_bf16_f32 v79, v44, v45
	global_store_dwordx2 v[50:51], v[78:79], off offset:3584
	s_nop 1
	v_div_scale_f32 v50, s[2:3], v80, v80, 1.0
	v_rcp_f32_e32 v51, v50
	s_nop 0
	v_fma_f32 v78, -v50, v51, 1.0
	v_fmac_f32_e32 v51, v78, v51
	v_div_scale_f32 v78, vcc, 1.0, v80, 1.0
	v_mul_f32_e32 v79, v78, v51
	v_fma_f32 v100, -v50, v79, v78
	v_fmac_f32_e32 v79, v100, v51
	v_fma_f32 v50, -v50, v79, v78
	v_div_fmas_f32 v50, v50, v51, v79
	v_div_fixup_f32 v50, v50, v80, 1.0
	v_pk_mul_f32 v[78:79], v[104:105], v[50:51] op_sel_hi:[1,0]
	v_pk_mul_f32 v[104:105], v[106:107], v[50:51] op_sel_hi:[1,0]
; #define GAS __attribute__((address_space(1)))
; __device__ __forceinline__ unsigned pk2(float lo, float hi) { f32x2_m v = {lo, hi}; bf16x2_m b = __builtin_convertvector(v, bf16x2_m); return __builtin_bit_cast(unsigned, b); }
; template <int MODE, bool W8 = false>
; __device__ __forceinline__ void norm_rows(const Ctx& C, const void* src, bf16* xdst, const unsigned char* YS8, const int* srow, const float* gate, const float* gain, bf16* XN, float* outf, unsigned char* XN8 = nullptr) {
;     ...
;             const GAS f32x4* gg = (const GAS f32x4*)gain + C.lane;
;             if (MODE <= 1) { GAS v2u* o = (GAS v2u*)(XN + (size_t)m * DM) + C.lane;
; #pragma unroll
;                 for (int j = 0; j < 8; ++j) { const f32x4 g = gg[64 * j]; const f32x4 y = v[q][j] * rstd * g; v2u w; w.x = pk2(y.x, y.y); w.y = pk2(y.z, y.w); o[64 * j] = w;
;                     if constexpr (W8) ((GAS unsigned*)(XN8 + (size_t)m * DM) + C.lane)[64 * j] = pk4_fp8m(y.x * SXN, y.y * SXN, y.z * SXN, y.w * SXN); } }
	v_add_co_u32_e32 v52, vcc, s16, v52
	v_pk_mul_f32 v[102:103], v[162:163], v[104:105]
	v_pk_mul_f32 v[78:79], v[160:161], v[78:79]
	v_cvt_pk_bf16_f32 v101, v102, v103
	v_cvt_pk_bf16_f32 v100, v78, v79
	v_addc_co_u32_e32 v53, vcc, 0, v53, vcc
	v_mul_f32_e32 v51, 0x42000000, v78
	v_mul_f32_e32 v78, 0x42000000, v79
	global_store_dwordx2 v[52:53], v[100:101], off
	s_nop 1
	v_med3_f32 v51, v51, s33, v214
	v_med3_f32 v78, v78, s33, v214
	v_mov_b32_e32 v100, v2
	v_cvt_pk_fp8_f32 v100, v51, v78
	v_mul_f32_e32 v79, 0x42000000, v102
	v_mul_f32_e32 v80, 0x42000000, v103
	v_med3_f32 v79, v79, s33, v214
	v_med3_f32 v80, v80, s33, v214
	v_cvt_pk_fp8_f32 v100, v79, v80 op_sel:[0,0,1]
	v_lshl_add_u64 v[78:79], s[4:5], 0, v[18:19]
	v_add_co_u32_e32 v78, vcc, s17, v78
	v_pk_mul_f32 v[74:75], v[74:75], v[50:51] op_sel_hi:[1,0]
	s_nop 0
	v_addc_co_u32_e32 v79, vcc, 0, v79, vcc
	global_store_dword v[78:79], v100, off
	s_nop 1
	v_pk_mul_f32 v[76:77], v[76:77], v[50:51] op_sel_hi:[1,0]
	v_lshl_add_u64 v[18:19], v[18:19], 0, s[18:19]
	v_pk_mul_f32 v[74:75], v[164:165], v[74:75]
	v_pk_mul_f32 v[76:77], v[166:167], v[76:77]
	v_cvt_pk_bf16_f32 v100, v74, v75
	v_mul_f32_e32 v51, 0x42000000, v74
	v_mul_f32_e32 v74, 0x42000000, v75
	v_cvt_pk_bf16_f32 v101, v76, v77
	v_mul_f32_e32 v75, 0x42000000, v76
	v_mul_f32_e32 v76, 0x42000000, v77
	v_med3_f32 v51, v51, s33, v214
	v_med3_f32 v74, v74, s33, v214
	v_mov_b32_e32 v77, v2
	v_cvt_pk_fp8_f32 v77, v51, v74
	v_med3_f32 v75, v75, s33, v214
	v_med3_f32 v76, v76, s33, v214
	global_store_dwordx2 v[52:53], v[100:101], off offset:512
	s_nop 1
	v_cvt_pk_fp8_f32 v77, v75, v76 op_sel:[0,0,1]
	v_pk_mul_f32 v[70:71], v[70:71], v[50:51] op_sel_hi:[1,0]
	v_pk_mul_f32 v[72:73], v[72:73], v[50:51] op_sel_hi:[1,0]
	global_store_dword v[78:79], v77, off offset:256
	s_nop 1
	v_pk_mul_f32 v[70:71], v[70:71], v[168:169]
	v_pk_mul_f32 v[72:73], v[72:73], v[170:171]
	v_cvt_pk_bf16_f32 v74, v70, v71
	v_mul_f32_e32 v51, 0x42000000, v70
	v_mul_f32_e32 v70, 0x42000000, v71
	v_cvt_pk_bf16_f32 v75, v72, v73
	v_mul_f32_e32 v71, 0x42000000, v72
	v_mul_f32_e32 v72, 0x42000000, v73
	v_med3_f32 v51, v51, s33, v214
	v_med3_f32 v70, v70, s33, v214
	v_mov_b32_e32 v73, v2
	v_cvt_pk_fp8_f32 v73, v51, v70
	v_med3_f32 v71, v71, s33, v214
	v_med3_f32 v72, v72, s33, v214
	global_store_dwordx2 v[52:53], v[74:75], off offset:1024
	s_nop 1
	v_cvt_pk_fp8_f32 v73, v71, v72 op_sel:[0,0,1]
	v_pk_mul_f32 v[66:67], v[66:67], v[50:51] op_sel_hi:[1,0]
	v_pk_mul_f32 v[68:69], v[68:69], v[50:51] op_sel_hi:[1,0]
	global_store_dword v[78:79], v73, off offset:512
	s_nop 1
	v_pk_mul_f32 v[66:67], v[66:67], v[172:173]
	v_pk_mul_f32 v[68:69], v[68:69], v[174:175]
	v_cvt_pk_bf16_f32 v70, v66, v67
	v_mul_f32_e32 v51, 0x42000000, v66
	v_mul_f32_e32 v66, 0x42000000, v67
	v_cvt_pk_bf16_f32 v71, v68, v69
	v_mul_f32_e32 v67, 0x42000000, v68
	v_mul_f32_e32 v68, 0x42000000, v69
	v_med3_f32 v51, v51, s33, v214
	v_med3_f32 v66, v66, s33, v214
	v_mov_b32_e32 v69, v2
	v_cvt_pk_fp8_f32 v69, v51, v66
	v_med3_f32 v67, v67, s33, v214
	v_med3_f32 v68, v68, s33, v214
	global_store_dwordx2 v[52:53], v[70:71], off offset:1536
	s_nop 1
	v_cvt_pk_fp8_f32 v69, v67, v68 op_sel:[0,0,1]
	v_pk_mul_f32 v[62:63], v[62:63], v[50:51] op_sel_hi:[1,0]
	v_pk_mul_f32 v[64:65], v[64:65], v[50:51] op_sel_hi:[1,0]
	global_store_dword v[78:79], v69, off offset:768
	s_nop 1
	v_pk_mul_f32 v[62:63], v[62:63], v[176:177]
	v_pk_mul_f32 v[64:65], v[64:65], v[178:179]
	v_cvt_pk_bf16_f32 v66, v62, v63
	v_mul_f32_e32 v51, 0x42000000, v62
	v_mul_f32_e32 v62, 0x42000000, v63
	v_cvt_pk_bf16_f32 v67, v64, v65
	v_mul_f32_e32 v63, 0x42000000, v64
	v_mul_f32_e32 v64, 0x42000000, v65
	v_med3_f32 v51, v51, s33, v214
	v_med3_f32 v62, v62, s33, v214
	v_mov_b32_e32 v65, v2
	v_cvt_pk_fp8_f32 v65, v51, v62
	v_med3_f32 v63, v63, s33, v214
	v_med3_f32 v64, v64, s33, v214
	global_store_dwordx2 v[52:53], v[66:67], off offset:2048
	s_nop 1
	v_cvt_pk_fp8_f32 v65, v63, v64 op_sel:[0,0,1]
	v_pk_mul_f32 v[58:59], v[58:59], v[50:51] op_sel_hi:[1,0]
	v_pk_mul_f32 v[60:61], v[60:61], v[50:51] op_sel_hi:[1,0]
	v_lshlrev_b32_e32 v66, 16, v22
	global_store_dword v[78:79], v65, off offset:1024
	s_nop 1
	v_and_b32_e32 v67, 0xffff0000, v22
	v_lshlrev_b32_e32 v22, 16, v23
	v_and_b32_e32 v23, 0xffff0000, v23
	v_lshlrev_b32_e32 v68, 16, v24
	v_and_b32_e32 v69, 0xffff0000, v24
	v_lshlrev_b32_e32 v24, 16, v25
	v_and_b32_e32 v25, 0xffff0000, v25
	v_pk_mul_f32 v[58:59], v[58:59], v[180:181]
	v_pk_mul_f32 v[60:61], v[60:61], v[182:183]
	v_cvt_pk_bf16_f32 v62, v58, v59
	v_mul_f32_e32 v51, 0x42000000, v58
	v_mul_f32_e32 v58, 0x42000000, v59
	v_cvt_pk_bf16_f32 v63, v60, v61
	v_mul_f32_e32 v59, 0x42000000, v60
	v_mul_f32_e32 v60, 0x42000000, v61
	v_med3_f32 v51, v51, s33, v214
	v_med3_f32 v58, v58, s33, v214
	v_mov_b32_e32 v61, v2
	v_cvt_pk_fp8_f32 v61, v51, v58
	v_med3_f32 v59, v59, s33, v214
	v_med3_f32 v60, v60, s33, v214
	global_store_dwordx2 v[52:53], v[62:63], off offset:2560
	s_nop 1
	v_cvt_pk_fp8_f32 v61, v59, v60 op_sel:[0,0,1]
	v_pk_mul_f32 v[46:47], v[46:47], v[50:51] op_sel_hi:[1,0]
	v_pk_mul_f32 v[48:49], v[48:49], v[50:51] op_sel_hi:[1,0]
	v_mov_b32_e32 v51, v2
	global_store_dword v[78:79], v61, off offset:1280
	s_nop 1
	v_pk_mul_f32 v[46:47], v[46:47], v[184:185]
	s_nop 0
	v_cvt_pk_bf16_f32 v58, v46, v47
	v_mul_f32_e32 v46, 0x42000000, v46
	v_mul_f32_e32 v47, 0x42000000, v47
	v_med3_f32 v46, v46, s33, v214
	v_med3_f32 v47, v47, s33, v214
	v_cvt_pk_fp8_f32 v51, v46, v47
	v_pk_mul_f32 v[48:49], v[48:49], v[186:187]
	v_lshlrev_b32_e32 v60, 16, v30
	v_cvt_pk_bf16_f32 v59, v48, v49
	v_mul_f32_e32 v48, 0x42000000, v48
	v_mul_f32_e32 v49, 0x42000000, v49
	v_med3_f32 v48, v48, s33, v214
	v_med3_f32 v49, v49, s33, v214
	v_cvt_pk_fp8_f32 v51, v48, v49 op_sel:[0,0,1]
	global_store_dwordx2 v[52:53], v[58:59], off offset:3072
	s_nop 1
	v_lshlrev_b32_e32 v58, 16, v32
	v_and_b32_e32 v59, 0xffff0000, v32
	global_store_dword v[78:79], v51, off offset:1536
	s_nop 1
	v_pk_mul_f32 v[42:43], v[42:43], v[50:51] op_sel_hi:[1,0]
	v_pk_mul_f32 v[44:45], v[44:45], v[50:51] op_sel_hi:[1,0]
	v_lshlrev_b32_e32 v50, 16, v40
	v_and_b32_e32 v51, 0xffff0000, v40
	v_lshlrev_b32_e32 v40, 16, v41
	v_and_b32_e32 v41, 0xffff0000, v41
	v_lshlrev_b32_e32 v32, 16, v33
	v_and_b32_e32 v33, 0xffff0000, v33
	v_and_b32_e32 v61, 0xffff0000, v30
	v_lshlrev_b32_e32 v30, 16, v31
	v_and_b32_e32 v31, 0xffff0000, v31
	v_pk_mul_f32 v[44:45], v[44:45], v[190:191]
	v_pk_mul_f32 v[42:43], v[42:43], v[188:189]
	v_cvt_pk_bf16_f32 v47, v44, v45
	v_cvt_pk_bf16_f32 v46, v42, v43
	v_mul_f32_e32 v42, 0x42000000, v42
	v_mul_f32_e32 v43, 0x42000000, v43
	global_store_dwordx2 v[52:53], v[46:47], off offset:3584
	s_nop 1
	v_med3_f32 v42, v42, s33, v214
	v_med3_f32 v43, v43, s33, v214
	v_mov_b32_e32 v46, v2
	v_cvt_pk_fp8_f32 v46, v42, v43
	v_mul_f32_e32 v44, 0x42000000, v44
	v_mul_f32_e32 v45, 0x42000000, v45
	v_med3_f32 v44, v44, s33, v214
	v_med3_f32 v45, v45, s33, v214
	v_cvt_pk_fp8_f32 v46, v44, v45 op_sel:[0,0,1]
	s_waitcnt vmcnt(23)
; template <int MODE, bool W8 = false>
; __device__ __forceinline__ void norm_rows(const Ctx& C, const void* src, bf16* xdst, const unsigned char* YS8, const int* srow, const float* gate, const float* gain, bf16* XN, float* outf, unsigned char* XN8 = nullptr) {
;     ...
;             if (MODE >= 1) {
; #pragma unroll
;                 for (int j = 0; j < 8; ++j) { const unsigned a = ya[q][j], b = yb[q][j];
;                     const f32x2_m a01 = __builtin_amdgcn_cvt_pk_f32_fp8((int)a, false), a23 = __builtin_amdgcn_cvt_pk_f32_fp8((int)a, true), b01 = __builtin_amdgcn_cvt_pk_f32_fp8((int)b, false), b23 = __builtin_amdgcn_cvt_pk_f32_fp8((int)b, true);
;                     v[q][j].x += h0[q] * a01.x + h1[q] * b01.x; v[q][j].y += h0[q] * a01.y + h1[q] * b01.y; v[q][j].z += h0[q] * a23.x + h1[q] * b23.x; v[q][j].w += h0[q] * a23.y + h1[q] * b23.y; } }
;             float ss = 0.f;
; #pragma unroll
;             for (int j = 0; j < 8; ++j) ss += (v[q][j].x * v[q][j].x + v[q][j].y * v[q][j].y) + (v[q][j].z * v[q][j].z + v[q][j].w * v[q][j].w);
	v_cvt_pk_f32_fp8_e32 v[42:43], v99
	v_cvt_pk_f32_fp8_sdwa v[48:49], v98 src0_sel:WORD_1
	v_cvt_pk_f32_fp8_sdwa v[44:45], v99 src0_sel:WORD_1
	global_store_dword v[78:79], v46, off offset:1792
	s_nop 1
	v_cvt_pk_f32_fp8_e32 v[46:47], v98
	v_pk_mul_f32 v[46:47], v[56:57], v[46:47] op_sel_hi:[0,1]
	v_pk_fma_f32 v[42:43], v[54:55], v[42:43], v[46:47] op_sel_hi:[0,1,1]
	v_pk_add_f32 v[62:63], v[42:43], v[50:51]
	v_pk_mul_f32 v[42:43], v[56:57], v[48:49] op_sel_hi:[0,1]
	v_pk_fma_f32 v[42:43], v[54:55], v[44:45], v[42:43] op_sel_hi:[0,1,1]
	v_cvt_pk_f32_fp8_e32 v[44:45], v96
	v_pk_add_f32 v[64:65], v[42:43], v[40:41]
	v_cvt_pk_f32_fp8_e32 v[40:41], v97
	v_cvt_pk_f32_fp8_sdwa v[46:47], v96 src0_sel:WORD_1
	v_cvt_pk_f32_fp8_sdwa v[42:43], v97 src0_sel:WORD_1
	v_pk_mul_f32 v[44:45], v[56:57], v[44:45] op_sel_hi:[0,1]
	v_lshlrev_b32_e32 v48, 16, v38
	v_and_b32_e32 v49, 0xffff0000, v38
	v_pk_fma_f32 v[40:41], v[54:55], v[40:41], v[44:45] op_sel_hi:[0,1,1]
	v_pk_add_f32 v[50:51], v[40:41], v[48:49]
	v_pk_mul_f32 v[40:41], v[56:57], v[46:47] op_sel_hi:[0,1]
	v_lshlrev_b32_e32 v38, 16, v39
	v_and_b32_e32 v39, 0xffff0000, v39
	v_pk_fma_f32 v[40:41], v[54:55], v[42:43], v[40:41] op_sel_hi:[0,1,1]
	v_cvt_pk_f32_fp8_e32 v[42:43], v94
	v_pk_add_f32 v[52:53], v[40:41], v[38:39]
	v_cvt_pk_f32_fp8_e32 v[38:39], v95
	v_cvt_pk_f32_fp8_sdwa v[44:45], v94 src0_sel:WORD_1
	v_cvt_pk_f32_fp8_sdwa v[40:41], v95 src0_sel:WORD_1
	v_pk_mul_f32 v[42:43], v[56:57], v[42:43] op_sel_hi:[0,1]
	v_lshlrev_b32_e32 v46, 16, v36
	v_and_b32_e32 v47, 0xffff0000, v36
	v_pk_fma_f32 v[38:39], v[54:55], v[38:39], v[42:43] op_sel_hi:[0,1,1]
	v_pk_add_f32 v[46:47], v[38:39], v[46:47]
	v_pk_mul_f32 v[38:39], v[56:57], v[44:45] op_sel_hi:[0,1]
	v_lshlrev_b32_e32 v36, 16, v37
	v_and_b32_e32 v37, 0xffff0000, v37
	v_pk_fma_f32 v[38:39], v[54:55], v[40:41], v[38:39] op_sel_hi:[0,1,1]
	v_cvt_pk_f32_fp8_e32 v[40:41], v92
	v_pk_add_f32 v[48:49], v[38:39], v[36:37]
	v_cvt_pk_f32_fp8_e32 v[36:37], v93
	v_cvt_pk_f32_fp8_sdwa v[44:45], v92 src0_sel:WORD_1
	v_cvt_pk_f32_fp8_sdwa v[38:39], v93 src0_sel:WORD_1
	v_pk_mul_f32 v[40:41], v[56:57], v[40:41] op_sel_hi:[0,1]
	v_lshlrev_b32_e32 v42, 16, v34
	v_and_b32_e32 v43, 0xffff0000, v34
	v_pk_fma_f32 v[36:37], v[54:55], v[36:37], v[40:41] op_sel_hi:[0,1,1]
	v_pk_add_f32 v[42:43], v[36:37], v[42:43]
	v_pk_mul_f32 v[36:37], v[56:57], v[44:45] op_sel_hi:[0,1]
	v_lshlrev_b32_e32 v34, 16, v35
	v_and_b32_e32 v35, 0xffff0000, v35
	v_pk_fma_f32 v[36:37], v[54:55], v[38:39], v[36:37] op_sel_hi:[0,1,1]
	v_cvt_pk_f32_fp8_e32 v[38:39], v90
	v_pk_add_f32 v[44:45], v[36:37], v[34:35]
	v_cvt_pk_f32_fp8_e32 v[34:35], v91
	v_cvt_pk_f32_fp8_sdwa v[40:41], v90 src0_sel:WORD_1
	v_cvt_pk_f32_fp8_sdwa v[36:37], v91 src0_sel:WORD_1
	v_pk_mul_f32 v[38:39], v[56:57], v[38:39] op_sel_hi:[0,1]
	v_pk_fma_f32 v[34:35], v[54:55], v[34:35], v[38:39] op_sel_hi:[0,1,1]
	v_pk_add_f32 v[38:39], v[34:35], v[58:59]
	v_pk_mul_f32 v[34:35], v[56:57], v[40:41] op_sel_hi:[0,1]
	v_pk_fma_f32 v[34:35], v[54:55], v[36:37], v[34:35] op_sel_hi:[0,1,1]
	v_pk_add_f32 v[40:41], v[34:35], v[32:33]
	v_cvt_pk_f32_fp8_e32 v[34:35], v88
	v_cvt_pk_f32_fp8_e32 v[32:33], v89
	v_cvt_pk_f32_fp8_sdwa v[58:59], v88 src0_sel:WORD_1
	v_cvt_pk_f32_fp8_sdwa v[36:37], v89 src0_sel:WORD_1
	v_pk_mul_f32 v[34:35], v[56:57], v[34:35] op_sel_hi:[0,1]
	v_pk_fma_f32 v[32:33], v[54:55], v[32:33], v[34:35] op_sel_hi:[0,1,1]
	v_pk_add_f32 v[34:35], v[32:33], v[60:61]
	v_pk_mul_f32 v[32:33], v[56:57], v[58:59] op_sel_hi:[0,1]
	v_pk_fma_f32 v[32:33], v[54:55], v[36:37], v[32:33] op_sel_hi:[0,1,1]
	v_cvt_pk_f32_fp8_e32 v[58:59], v86
	v_pk_add_f32 v[36:37], v[32:33], v[30:31]
	v_cvt_pk_f32_fp8_e32 v[30:31], v87
	v_cvt_pk_f32_fp8_sdwa v[60:61], v86 src0_sel:WORD_1
	v_cvt_pk_f32_fp8_sdwa v[32:33], v87 src0_sel:WORD_1
	v_pk_mul_f32 v[58:59], v[56:57], v[58:59] op_sel_hi:[0,1]
	v_pk_fma_f32 v[30:31], v[54:55], v[30:31], v[58:59] op_sel_hi:[0,1,1]
	v_pk_mul_f32 v[58:59], v[56:57], v[60:61] op_sel_hi:[0,1]
	v_pk_fma_f32 v[32:33], v[54:55], v[32:33], v[58:59] op_sel_hi:[0,1,1]
	v_cvt_pk_f32_fp8_e32 v[60:61], v55
	v_pk_add_f32 v[30:31], v[30:31], v[66:67]
	v_pk_add_f32 v[32:33], v[32:33], v[22:23]
	v_cvt_pk_f32_fp8_e32 v[22:23], v85
	v_cvt_pk_f32_fp8_sdwa v[66:67], v55 src0_sel:WORD_1
	v_cvt_pk_f32_fp8_sdwa v[58:59], v85 src0_sel:WORD_1
	v_pk_mul_f32 v[60:61], v[56:57], v[60:61] op_sel_hi:[0,1]
	v_pk_fma_f32 v[22:23], v[54:55], v[22:23], v[60:61] op_sel_hi:[0,1,1]
	v_pk_mul_f32 v[60:61], v[56:57], v[66:67] op_sel_hi:[0,1]
	v_pk_fma_f32 v[54:55], v[54:55], v[58:59], v[60:61] op_sel_hi:[0,1,1]
	v_mov_b32_e32 v58, v63
	v_mov_b32_e32 v59, v51
	v_pk_add_f32 v[24:25], v[54:55], v[24:25]
	v_mov_b32_e32 v54, v62
	v_mov_b32_e32 v55, v50
	v_pk_mul_f32 v[58:59], v[58:59], v[58:59]
	v_mov_b32_e32 v60, v65
	v_mov_b32_e32 v61, v53
	v_pk_fma_f32 v[54:55], v[54:55], v[54:55], v[58:59]
	v_mov_b32_e32 v58, v64
	v_mov_b32_e32 v59, v52
	v_pk_mul_f32 v[60:61], v[60:61], v[60:61]
	v_mul_f32_e32 v56, v43, v43
	v_pk_fma_f32 v[58:59], v[58:59], v[58:59], v[60:61]
	v_mov_b32_e32 v60, v47
	v_mov_b32_e32 v61, v49
	v_pk_add_f32 v[54:55], v[54:55], v[58:59]
	v_mov_b32_e32 v58, v46
	v_mov_b32_e32 v59, v48
	v_pk_mul_f32 v[60:61], v[60:61], v[60:61]
	v_pk_add_f32 v[22:23], v[22:23], v[68:69]
	v_pk_fma_f32 v[58:59], v[58:59], v[58:59], v[60:61]
	v_pk_fma_f32 v[60:61], v[42:43], v[42:43], v[56:57] op_sel_hi:[1,1,0]
	v_mul_f32_e32 v56, v45, v45
	v_pk_add_f32 v[54:55], v[54:55], v[54:55] op_sel:[0,1] op_sel_hi:[1,0]
	v_pk_add_f32 v[58:59], v[58:59], v[58:59] op_sel:[0,1] op_sel_hi:[1,0]
	v_pk_fma_f32 v[66:67], v[44:45], v[44:45], v[56:57] op_sel_hi:[1,1,0]
	v_pk_mul_f32 v[68:69], v[38:39], v[38:39]
	v_pk_mul_f32 v[70:71], v[40:41], v[40:41]
	v_mov_b32_e32 v55, v68
	v_mov_b32_e32 v59, v69
	v_mov_b32_e32 v61, v70
	v_mov_b32_e32 v67, v71
	v_pk_add_f32 v[54:55], v[54:55], v[58:59]
	v_pk_add_f32 v[58:59], v[60:61], v[66:67]
	v_mov_b32_e32 v60, v35
	v_mov_b32_e32 v61, v37
	v_pk_add_f32 v[54:55], v[54:55], v[58:59]
	v_mov_b32_e32 v58, v34
	v_mov_b32_e32 v59, v36
	v_pk_mul_f32 v[60:61], v[60:61], v[60:61]
	v_mul_f32_e32 v56, v31, v31
	v_pk_fma_f32 v[58:59], v[58:59], v[58:59], v[60:61]
	v_pk_fma_f32 v[60:61], v[30:31], v[30:31], v[56:57] op_sel_hi:[1,1,0]
	v_mul_f32_e32 v56, v33, v33
	v_pk_add_f32 v[54:55], v[54:55], v[54:55] op_sel:[0,1] op_sel_hi:[1,0]
	v_pk_add_f32 v[58:59], v[58:59], v[58:59] op_sel:[0,1] op_sel_hi:[1,0]
	v_pk_fma_f32 v[66:67], v[32:33], v[32:33], v[56:57] op_sel_hi:[1,1,0]
	v_pk_mul_f32 v[68:69], v[22:23], v[22:23]
	v_pk_mul_f32 v[70:71], v[24:25], v[24:25]
	v_mov_b32_e32 v55, v68
	v_mov_b32_e32 v59, v69
	v_mov_b32_e32 v61, v70
	v_mov_b32_e32 v67, v71
	v_pk_add_f32 v[54:55], v[54:55], v[58:59]
	v_pk_add_f32 v[58:59], v[60:61], v[66:67]
	s_nop 0
	v_pk_add_f32 v[54:55], v[54:55], v[58:59]
	s_nop 0
	v_add_f32_e32 v54, v54, v55
	ds_bpermute_b32 v55, v3, v54
	s_waitcnt lgkmcnt(0)
; #define GAS __attribute__((address_space(1)))
; __device__ __forceinline__ unsigned pk2(float lo, float hi) { f32x2_m v = {lo, hi}; bf16x2_m b = __builtin_convertvector(v, bf16x2_m); return __builtin_bit_cast(unsigned, b); }
; template <int MODE, bool W8 = false>
; __device__ __forceinline__ void norm_rows(const Ctx& C, const void* src, bf16* xdst, const unsigned char* YS8, const int* srow, const float* gate, const float* gain, bf16* XN, float* outf, unsigned char* XN8 = nullptr) {
;     ...
;             const float rstd = 1.0f / sqrtf(wave_sum(ss) * (1.0f / DM) + RMS_EPS);
;             if (MODE == 1) { GAS v2u* xo = (GAS v2u*)(xdst + (size_t)m * DM) + C.lane;
; #pragma unroll
;                 for (int j = 0; j < 8; ++j) { v2u w; w.x = pk2(v[q][j].x, v[q][j].y); w.y = pk2(v[q][j].z, v[q][j].w); xo[64 * j] = w; } }
;             const GAS f32x4* gg = (const GAS f32x4*)gain + C.lane;
;             if (MODE <= 1) { GAS v2u* o = (GAS v2u*)(XN + (size_t)m * DM) + C.lane;
; #pragma unroll
;                 for (int j = 0; j < 8; ++j) { const f32x4 g = gg[64 * j]; const f32x4 y = v[q][j] * rstd * g; v2u w; w.x = pk2(y.x, y.y); w.y = pk2(y.z, y.w); o[64 * j] = w;
;                     if constexpr (W8) ((GAS unsigned*)(XN8 + (size_t)m * DM) + C.lane)[64 * j] = pk4_fp8m(y.x * SXN, y.y * SXN, y.z * SXN, y.w * SXN); } }
	v_add_f32_e32 v54, v54, v55
	ds_bpermute_b32 v55, v57, v54
	s_waitcnt lgkmcnt(0)
	v_add_f32_e32 v54, v54, v55
	ds_bpermute_b32 v55, v81, v54
	s_waitcnt lgkmcnt(0)
	v_add_f32_e32 v54, v54, v55
	ds_bpermute_b32 v55, v82, v54
	s_waitcnt lgkmcnt(0)
	v_add_f32_e32 v54, v54, v55
	ds_bpermute_b32 v55, v83, v54
	s_waitcnt lgkmcnt(0)
	v_add_f32_e32 v54, v54, v55
	ds_bpermute_b32 v55, v84, v54
	s_waitcnt lgkmcnt(0)
	v_add_f32_e32 v54, v54, v55
	v_fmamk_f32 v54, v54, 0x3a000000, v212
	v_cmp_gt_f32_e32 vcc, s12, v54
	v_mul_f32_e32 v55, 0x4f800000, v54
	s_nop 0
	v_cndmask_b32_e32 v54, v54, v55, vcc
	v_sqrt_f32_e32 v55, v54
	s_nop 0
	v_add_u32_e32 v56, -1, v55
	v_fma_f32 v58, -v56, v55, v54
	v_cmp_ge_f32_e64 s[2:3], 0, v58
	v_add_u32_e32 v58, 1, v55
	s_nop 0
	v_cndmask_b32_e64 v56, v55, v56, s[2:3]
	v_fma_f32 v55, -v58, v55, v54
	v_cmp_lt_f32_e64 s[2:3], 0, v55
	s_nop 1
	v_cndmask_b32_e64 v55, v56, v58, s[2:3]
	v_mul_f32_e32 v56, 0x37800000, v55
	v_cndmask_b32_e32 v55, v55, v56, vcc
	v_cmp_class_f32_e32 vcc, v54, v211
	s_nop 1
	v_cndmask_b32_e32 v56, v55, v54, vcc
	v_cvt_pk_bf16_f32 v54, v62, v63
	v_cvt_pk_bf16_f32 v55, v64, v65
	global_store_dwordx2 v[26:27], v[54:55], off
	s_nop 1
	v_cvt_pk_bf16_f32 v54, v50, v51
	v_cvt_pk_bf16_f32 v55, v52, v53
	global_store_dwordx2 v[26:27], v[54:55], off offset:512
	s_nop 1
	v_cvt_pk_bf16_f32 v54, v46, v47
	v_cvt_pk_bf16_f32 v55, v48, v49
	global_store_dwordx2 v[26:27], v[54:55], off offset:1024
	s_nop 1
	v_cvt_pk_bf16_f32 v54, v42, v43
	v_cvt_pk_bf16_f32 v55, v44, v45
	global_store_dwordx2 v[26:27], v[54:55], off offset:1536
	s_nop 1
	v_cvt_pk_bf16_f32 v54, v38, v39
	v_cvt_pk_bf16_f32 v55, v40, v41
	global_store_dwordx2 v[26:27], v[54:55], off offset:2048
	s_nop 1
	v_cvt_pk_bf16_f32 v54, v34, v35
	v_cvt_pk_bf16_f32 v55, v36, v37
	global_store_dwordx2 v[26:27], v[54:55], off offset:2560
	s_nop 1
	v_cvt_pk_bf16_f32 v54, v30, v31
	v_cvt_pk_bf16_f32 v55, v32, v33
	global_store_dwordx2 v[26:27], v[54:55], off offset:3072
	s_nop 1
	v_cvt_pk_bf16_f32 v54, v22, v23
	v_cvt_pk_bf16_f32 v55, v24, v25
	global_store_dwordx2 v[26:27], v[54:55], off offset:3584
	s_nop 1
	v_div_scale_f32 v26, s[2:3], v56, v56, 1.0
	v_rcp_f32_e32 v27, v26
	s_nop 0
	v_fma_f32 v54, -v26, v27, 1.0
	v_fmac_f32_e32 v27, v54, v27
	v_div_scale_f32 v54, vcc, 1.0, v56, 1.0
	v_mul_f32_e32 v55, v54, v27
	v_fma_f32 v58, -v26, v55, v54
	v_fmac_f32_e32 v55, v58, v27
	v_fma_f32 v26, -v26, v55, v54
	v_div_fmas_f32 v26, v26, v27, v55
	v_div_fixup_f32 v26, v26, v56, 1.0
	v_pk_mul_f32 v[54:55], v[62:63], v[26:27] op_sel_hi:[1,0]
	v_pk_mul_f32 v[62:63], v[64:65], v[26:27] op_sel_hi:[1,0]
	v_add_co_u32_e32 v28, vcc, s16, v28
	v_pk_mul_f32 v[54:55], v[160:161], v[54:55]
	s_nop 0
	v_cvt_pk_bf16_f32 v58, v54, v55
	v_mul_f32_e32 v27, 0x42000000, v54
	v_mul_f32_e32 v55, 0x42000000, v55
	v_med3_f32 v54, v27, s33, v214
	v_med3_f32 v55, v55, s33, v214
	v_mov_b32_e32 v27, v2
	v_pk_mul_f32 v[60:61], v[162:163], v[62:63]
	v_cvt_pk_fp8_f32 v27, v54, v55
	v_cvt_pk_bf16_f32 v59, v60, v61
	v_addc_co_u32_e32 v29, vcc, 0, v29, vcc
	global_store_dwordx2 v[28:29], v[58:59], off
	s_nop 1
	v_mul_f32_e32 v56, 0x42000000, v60
	v_mul_f32_e32 v58, 0x42000000, v61
	v_med3_f32 v56, v56, s33, v214
	v_med3_f32 v58, v58, s33, v214
	v_cvt_pk_fp8_f32 v27, v56, v58 op_sel:[0,0,1]
	v_lshl_add_u64 v[54:55], s[4:5], 0, v[14:15]
	v_add_co_u32_e32 v54, vcc, s17, v54
	v_pk_mul_f32 v[50:51], v[50:51], v[26:27] op_sel_hi:[1,0]
	s_nop 0
	v_addc_co_u32_e32 v55, vcc, 0, v55, vcc
	global_store_dword v[54:55], v27, off
	s_nop 1
	v_pk_mul_f32 v[52:53], v[52:53], v[26:27] op_sel_hi:[1,0]
	v_lshl_add_u64 v[14:15], v[14:15], 0, s[18:19]
	v_pk_mul_f32 v[50:51], v[164:165], v[50:51]
	v_pk_mul_f32 v[52:53], v[166:167], v[52:53]
	v_cvt_pk_bf16_f32 v58, v50, v51
	v_mul_f32_e32 v27, 0x42000000, v50
	v_mul_f32_e32 v50, 0x42000000, v51
	v_cvt_pk_bf16_f32 v59, v52, v53
	v_mul_f32_e32 v51, 0x42000000, v52
	v_mul_f32_e32 v52, 0x42000000, v53
	v_med3_f32 v27, v27, s33, v214
	v_med3_f32 v50, v50, s33, v214
	v_mov_b32_e32 v53, v2
	v_cvt_pk_fp8_f32 v53, v27, v50
	v_med3_f32 v51, v51, s33, v214
	v_med3_f32 v52, v52, s33, v214
	global_store_dwordx2 v[28:29], v[58:59], off offset:512
	s_nop 1
	v_cvt_pk_fp8_f32 v53, v51, v52 op_sel:[0,0,1]
	v_pk_mul_f32 v[46:47], v[46:47], v[26:27] op_sel_hi:[1,0]
	v_pk_mul_f32 v[48:49], v[48:49], v[26:27] op_sel_hi:[1,0]
	global_store_dword v[54:55], v53, off offset:256
	s_nop 1
	v_pk_mul_f32 v[46:47], v[46:47], v[168:169]
	v_pk_mul_f32 v[48:49], v[48:49], v[170:171]
; #define GAS __attribute__((address_space(1)))
; __device__ __forceinline__ unsigned pk2(float lo, float hi) { f32x2_m v = {lo, hi}; bf16x2_m b = __builtin_convertvector(v, bf16x2_m); return __builtin_bit_cast(unsigned, b); }
; template <int MODE, bool W8 = false>
; __device__ __forceinline__ void norm_rows(const Ctx& C, const void* src, bf16* xdst, const unsigned char* YS8, const int* srow, const float* gate, const float* gain, bf16* XN, float* outf, unsigned char* XN8 = nullptr) {
;     ...
;             const GAS f32x4* gg = (const GAS f32x4*)gain + C.lane;
;             if (MODE <= 1) { GAS v2u* o = (GAS v2u*)(XN + (size_t)m * DM) + C.lane;
; #pragma unroll
;                 for (int j = 0; j < 8; ++j) { const f32x4 g = gg[64 * j]; const f32x4 y = v[q][j] * rstd * g; v2u w; w.x = pk2(y.x, y.y); w.y = pk2(y.z, y.w); o[64 * j] = w;
;                     if constexpr (W8) ((GAS unsigned*)(XN8 + (size_t)m * DM) + C.lane)[64 * j] = pk4_fp8m(y.x * SXN, y.y * SXN, y.z * SXN, y.w * SXN); } }
	v_cvt_pk_bf16_f32 v50, v46, v47
	v_mul_f32_e32 v27, 0x42000000, v46
	v_mul_f32_e32 v46, 0x42000000, v47
	v_cvt_pk_bf16_f32 v51, v48, v49
	v_mul_f32_e32 v47, 0x42000000, v48
	v_mul_f32_e32 v48, 0x42000000, v49
	v_med3_f32 v27, v27, s33, v214
	v_med3_f32 v46, v46, s33, v214
	v_mov_b32_e32 v49, v2
	v_cvt_pk_fp8_f32 v49, v27, v46
	v_med3_f32 v47, v47, s33, v214
	v_med3_f32 v48, v48, s33, v214
	global_store_dwordx2 v[28:29], v[50:51], off offset:1024
	s_nop 1
	v_cvt_pk_fp8_f32 v49, v47, v48 op_sel:[0,0,1]
	v_pk_mul_f32 v[42:43], v[42:43], v[26:27] op_sel_hi:[1,0]
	v_pk_mul_f32 v[44:45], v[44:45], v[26:27] op_sel_hi:[1,0]
	global_store_dword v[54:55], v49, off offset:512
	s_nop 1
	v_pk_mul_f32 v[42:43], v[42:43], v[172:173]
	v_pk_mul_f32 v[44:45], v[44:45], v[174:175]
	v_cvt_pk_bf16_f32 v46, v42, v43
	v_mul_f32_e32 v27, 0x42000000, v42
	v_mul_f32_e32 v42, 0x42000000, v43
	v_cvt_pk_bf16_f32 v47, v44, v45
	v_mul_f32_e32 v43, 0x42000000, v44
	v_mul_f32_e32 v44, 0x42000000, v45
	v_med3_f32 v27, v27, s33, v214
	v_med3_f32 v42, v42, s33, v214
	v_mov_b32_e32 v45, v2
	v_cvt_pk_fp8_f32 v45, v27, v42
	v_med3_f32 v43, v43, s33, v214
	v_med3_f32 v44, v44, s33, v214
	global_store_dwordx2 v[28:29], v[46:47], off offset:1536
	s_nop 1
	v_cvt_pk_fp8_f32 v45, v43, v44 op_sel:[0,0,1]
	v_pk_mul_f32 v[38:39], v[38:39], v[26:27] op_sel_hi:[1,0]
	v_pk_mul_f32 v[40:41], v[40:41], v[26:27] op_sel_hi:[1,0]
	global_store_dword v[54:55], v45, off offset:768
	s_nop 1
	v_pk_mul_f32 v[38:39], v[38:39], v[176:177]
	v_pk_mul_f32 v[40:41], v[40:41], v[178:179]
	v_cvt_pk_bf16_f32 v42, v38, v39
	v_mul_f32_e32 v27, 0x42000000, v38
	v_mul_f32_e32 v38, 0x42000000, v39
	v_cvt_pk_bf16_f32 v43, v40, v41
	v_mul_f32_e32 v39, 0x42000000, v40
	v_mul_f32_e32 v40, 0x42000000, v41
	v_med3_f32 v27, v27, s33, v214
	v_med3_f32 v38, v38, s33, v214
	v_mov_b32_e32 v41, v2
	v_cvt_pk_fp8_f32 v41, v27, v38
	v_med3_f32 v39, v39, s33, v214
	v_med3_f32 v40, v40, s33, v214
	global_store_dwordx2 v[28:29], v[42:43], off offset:2048
	s_nop 1
	v_cvt_pk_fp8_f32 v41, v39, v40 op_sel:[0,0,1]
	v_pk_mul_f32 v[34:35], v[34:35], v[26:27] op_sel_hi:[1,0]
	v_pk_mul_f32 v[36:37], v[36:37], v[26:27] op_sel_hi:[1,0]
	global_store_dword v[54:55], v41, off offset:1024
	s_nop 1
	v_pk_mul_f32 v[34:35], v[34:35], v[180:181]
	v_pk_mul_f32 v[36:37], v[36:37], v[182:183]
	v_cvt_pk_bf16_f32 v38, v34, v35
	v_mul_f32_e32 v27, 0x42000000, v34
	v_mul_f32_e32 v34, 0x42000000, v35
	v_cvt_pk_bf16_f32 v39, v36, v37
	v_mul_f32_e32 v35, 0x42000000, v36
	v_mul_f32_e32 v36, 0x42000000, v37
	v_med3_f32 v27, v27, s33, v214
	v_med3_f32 v34, v34, s33, v214
	v_mov_b32_e32 v37, v2
	v_cvt_pk_fp8_f32 v37, v27, v34
	v_med3_f32 v35, v35, s33, v214
	v_med3_f32 v36, v36, s33, v214
	global_store_dwordx2 v[28:29], v[38:39], off offset:2560
	s_nop 1
	v_cvt_pk_fp8_f32 v37, v35, v36 op_sel:[0,0,1]
	v_pk_mul_f32 v[30:31], v[30:31], v[26:27] op_sel_hi:[1,0]
	v_pk_mul_f32 v[32:33], v[32:33], v[26:27] op_sel_hi:[1,0]
	global_store_dword v[54:55], v37, off offset:1280
	s_nop 1
	v_pk_mul_f32 v[30:31], v[30:31], v[184:185]
	v_pk_mul_f32 v[32:33], v[32:33], v[186:187]
	v_cvt_pk_bf16_f32 v34, v30, v31
	v_mul_f32_e32 v27, 0x42000000, v30
	v_mul_f32_e32 v30, 0x42000000, v31
	v_cvt_pk_bf16_f32 v35, v32, v33
	v_mul_f32_e32 v31, 0x42000000, v32
	v_mul_f32_e32 v32, 0x42000000, v33
	v_med3_f32 v27, v27, s33, v214
	v_med3_f32 v30, v30, s33, v214
	v_mov_b32_e32 v33, v2
	v_cvt_pk_fp8_f32 v33, v27, v30
	v_med3_f32 v31, v31, s33, v214
	v_med3_f32 v32, v32, s33, v214
	global_store_dwordx2 v[28:29], v[34:35], off offset:3072
	s_nop 1
	v_cvt_pk_fp8_f32 v33, v31, v32 op_sel:[0,0,1]
	v_pk_mul_f32 v[22:23], v[22:23], v[26:27] op_sel_hi:[1,0]
	v_pk_mul_f32 v[24:25], v[24:25], v[26:27] op_sel_hi:[1,0]
	global_store_dword v[54:55], v33, off offset:1536
	s_nop 1
	v_pk_mul_f32 v[24:25], v[24:25], v[190:191]
	v_pk_mul_f32 v[22:23], v[22:23], v[188:189]
	v_cvt_pk_bf16_f32 v27, v24, v25
	v_cvt_pk_bf16_f32 v26, v22, v23
	v_mul_f32_e32 v22, 0x42000000, v22
	v_mul_f32_e32 v23, 0x42000000, v23
	global_store_dwordx2 v[28:29], v[26:27], off offset:3584
	s_nop 1
	v_med3_f32 v22, v22, s33, v214
	v_med3_f32 v23, v23, s33, v214
	v_mov_b32_e32 v26, v2
	v_cvt_pk_fp8_f32 v26, v22, v23
	v_mul_f32_e32 v24, 0x42000000, v24
	v_mul_f32_e32 v25, 0x42000000, v25
	v_med3_f32 v24, v24, s33, v214
	v_med3_f32 v25, v25, s33, v214
	v_cvt_pk_fp8_f32 v26, v24, v25 op_sel:[0,0,1]
	global_store_dword v[54:55], v26, off offset:1792
	s_nop 1
	s_cbranch_scc0 .LBB0_1326
